# GEMM K-loops (in-proj, gate_up, down): first trip peeled with C=0 MFMAs, the 128 accumulator-zeroing v_mov per unit removed
# speedup vs baseline: 1.0129x; 1.0075x over previous
; #define PG8_STAGE_A(bufoff, kbase, h, gv) do { if constexpr (GATHER) { PG8_STAGE(bufoff, kbase, (gv)[h]); } else { PG8_STAGE(bufoff, (kbase) + (h) * hstep, voffA); } } while (0)
; #define PG8_WAIT_V(n) asm volatile("s_waitcnt vmcnt(" #n ")" ::: "memory")
; template <class Epi, class Sched, bool ALIGN_EPI = false, bool SP2 = false, bool FP8 = false, bool GATHER = false>
; __device__ __forceinline__ void gemm_phase(PG8_LAS unsigned char* lds, const Gemm g, const Sched& S, const Epi& E) {
;     ...
;         const bool has_next = S.next(ui + 1, nxt);
;         const char* nA = (has_next && !GATHER) ? (const char*)g.A + (size_t)nxt.pm * tstep : cA; const char* nB = has_next ? (const char*)g.Bt + (size_t)S.brow(nxt) * (size_t)K * 2 : cB;
; #pragma nounroll
;         for (int t = 0; t < nt; t += 2) {
;             const bool last = (t == nt - 2);
;             const char* a1 = cA + (size_t)(t + 1) * kstep;
;             const char* a2 = last ? nA : cA + (size_t)(t + 2) * kstep; const char* b2 = last ? nB : cB + (size_t)(t + 2) * kstep;
;             const char* a3 = a2 + kstep; const char* b3 = b2 + kstep;
;             if (last && has_next) S.a_ready(nxt);
;             if (last) E.pre(cur, wid, lane);
;             if constexpr (GATHER) { if (t == nt - 4 && has_next) { _Pragma("unroll") for (int h_ = 0; h_ < 2; ++h_) _Pragma("unroll") for (int i_ = 0; i_ < 2; ++i_)
;                 asm volatile("global_load_dword %0, %1, off" : "+v"(graw[h_][i_]) : "v"(S.rowtok + (nxt.pm * BM + h_ * HALF + gR[i_])) : "memory"); } }
;             unsigned gsel[2][2];
;             if constexpr (GATHER) { _Pragma("unroll") for (int h_ = 0; h_ < 2; ++h_) _Pragma("unroll") for (int i_ = 0; i_ < 2; ++i_) { if (last && has_next) gnxt[h_][i_] = graw[h_][i_] * (unsigned)(K * 2) + gC[i_]; gsel[h_][i_] = (last && has_next) ? gnxt[h_][i_] : gcur[h_][i_]; } }
;             if constexpr (SP2) {
;             PG8_LDB(B0, 0, 0); PG8_LDB(B1, 0, 1); PG8_SCHED; PG8_LDA(At, 0, 0); PG8_STAGE_A(PG8_SA(1, 1), a1, 1, gcur);
;             PG8_WAIT_V(8); PG8_WAIT_L(0); PG8_BAR; PG8_MMA(0, 0, At, B0); PG8_MMA(0, 1, At, B1); PG8_BAR; PG8_SCHED;
;             PG8_LDA(At, 0, 1); PG8_STAGE(PG8_SB(0, 0), b2, voffB); PG8_STAGE(PG8_SB(0, 1), b2 + hstep, voffB); PG8_STAGE_A(PG8_SA(0, 0), a2, 0, gsel);
;             PG8_WAIT_V(8); PG8_WAIT_L(0); PG8_BAR; PG8_MMA(1, 0, At, B0); PG8_MMA(1, 1, At, B1); PG8_BAR; PG8_SCHED;
.LBB0_222:
	s_mov_b32 s44, s5
	s_ashr_i32 s45, s5, 31
	s_lshl_b64 s[10:11], s[44:45], 19
	s_add_u32 s48, s65, s10
	s_addc_u32 s49, s66, s11
	s_mov_b32 s93, s12
	s_and_b64 s[10:11], s[46:47], exec
	s_cselect_b32 s5, s49, s7
	s_cselect_b32 s12, s48, s6
	s_lshl_b32 s10, s93, 8
	s_ashr_i32 s11, s10, 31
	s_lshl_b64 s[10:11], s[10:11], 11
	s_add_u32 s50, s62, s10
	s_addc_u32 s51, s63, s11
	s_and_b64 s[10:11], s[46:47], exec
	s_cselect_b32 s13, s51, s9
	s_cselect_b32 s14, s50, s8
	s_add_u32 s6, s6, 0x40080
	s_addc_u32 s7, s7, 0
	s_add_u32 s15, s8, 0x100
	s_addc_u32 s16, s9, 0
	s_mov_b32 s45, -2
	ds_read_b128 v[74:77], v164
	ds_read_b128 v[78:81], v164 offset:1024
	ds_read_b128 v[152:155], v164 offset:2048
	ds_read_b128 v[156:159], v164 offset:3072
	ds_read_b128 v[170:173], v165
	ds_read_b128 v[174:177], v165 offset:1024
	ds_read_b128 v[178:181], v165 offset:2048
	ds_read_b128 v[182:185], v165 offset:3072
	s_add_u32 s8, s6, 0xfffc0080
	s_addc_u32 s9, s7, -1
	s_cmp_eq_u32 s45, 12
	s_cselect_b32 s11, s5, s9
	s_cselect_b32 s10, s12, s8
	s_cselect_b32 s9, s13, s16
	s_cselect_b32 s8, s14, s15
	v_lshl_add_u64 v[160:161], s[6:7], 0, v[146:147]
	s_add_i32 m0, s67, 0xc000
	ds_read_b128 v[186:189], v166
	ds_read_b128 v[190:193], v166 offset:1024
	ds_read_b128 v[194:197], v166 offset:2048
	ds_read_b128 v[198:201], v166 offset:3072
	ds_read_b128 v[202:205], v166 offset:4096
	ds_read_b128 v[206:209], v166 offset:5120
	ds_read_b128 v[210:213], v166 offset:6144
	ds_read_b128 v[214:217], v166 offset:7168
	global_load_lds_dwordx4 v[160:161], off
	v_lshl_add_u64 v[160:161], s[6:7], 0, v[148:149]
	s_add_i32 m0, s67, 0xe000
	s_nop 0
	global_load_lds_dwordx4 v[160:161], off
	s_waitcnt vmcnt(8)
	s_waitcnt lgkmcnt(0)
	s_barrier
	s_setprio 1
	s_waitcnt lgkmcnt(0)
	v_mfma_f32_16x16x32_bf16 v[134:137], v[74:77], v[186:189], 0
	v_mfma_f32_16x16x32_bf16 v[130:133], v[152:155], v[186:189], 0
	v_mfma_f32_16x16x32_bf16 v[126:129], v[74:77], v[194:197], 0
	v_mfma_f32_16x16x32_bf16 v[122:125], v[152:155], v[194:197], 0
	v_mfma_f32_16x16x32_bf16 v[118:121], v[74:77], v[202:205], 0
	v_mfma_f32_16x16x32_bf16 v[114:117], v[152:155], v[202:205], 0
	v_mfma_f32_16x16x32_bf16 v[110:113], v[74:77], v[210:213], 0
	v_mfma_f32_16x16x32_bf16 v[106:109], v[152:155], v[210:213], 0
	v_mfma_f32_16x16x32_bf16 v[134:137], v[78:81], v[190:193], v[134:137]
	v_mfma_f32_16x16x32_bf16 v[130:133], v[156:159], v[190:193], v[130:133]
	v_mfma_f32_16x16x32_bf16 v[126:129], v[78:81], v[198:201], v[126:129]
	v_mfma_f32_16x16x32_bf16 v[122:125], v[156:159], v[198:201], v[122:125]
	v_mfma_f32_16x16x32_bf16 v[118:121], v[78:81], v[206:209], v[118:121]
	v_mfma_f32_16x16x32_bf16 v[114:117], v[156:159], v[206:209], v[114:117]
	v_mfma_f32_16x16x32_bf16 v[110:113], v[78:81], v[214:217], v[110:113]
	v_mfma_f32_16x16x32_bf16 v[106:109], v[156:159], v[214:217], v[106:109]
	s_setprio 0
	s_setprio 1
	v_mfma_f32_16x16x32_bf16 v[62:65], v[170:173], v[186:189], 0
	v_mfma_f32_16x16x32_bf16 v[58:61], v[178:181], v[186:189], 0
	v_mfma_f32_16x16x32_bf16 v[54:57], v[170:173], v[194:197], 0
	v_mfma_f32_16x16x32_bf16 v[50:53], v[178:181], v[194:197], 0
	v_mfma_f32_16x16x32_bf16 v[46:49], v[170:173], v[202:205], 0
	v_mfma_f32_16x16x32_bf16 v[42:45], v[178:181], v[202:205], 0
	v_mfma_f32_16x16x32_bf16 v[38:41], v[170:173], v[210:213], 0
	v_mfma_f32_16x16x32_bf16 v[34:37], v[178:181], v[210:213], 0
	v_mfma_f32_16x16x32_bf16 v[62:65], v[174:177], v[190:193], v[62:65]
	v_mfma_f32_16x16x32_bf16 v[58:61], v[182:185], v[190:193], v[58:61]
	v_mfma_f32_16x16x32_bf16 v[54:57], v[174:177], v[198:201], v[54:57]
	v_mfma_f32_16x16x32_bf16 v[50:53], v[182:185], v[198:201], v[50:53]
	v_mfma_f32_16x16x32_bf16 v[46:49], v[174:177], v[206:209], v[46:49]
	v_mfma_f32_16x16x32_bf16 v[42:45], v[182:185], v[206:209], v[42:45]
	v_mfma_f32_16x16x32_bf16 v[38:41], v[174:177], v[214:217], v[38:41]
	v_mfma_f32_16x16x32_bf16 v[34:37], v[182:185], v[214:217], v[34:37]
	s_setprio 0
	s_barrier
	s_add_i32 s53, s85, s35
	v_lshl_add_u64 v[160:161], s[8:9], 0, v[140:141]
	s_mov_b32 m0, s53
	ds_read_b128 v[186:189], v166 offset:16384
	ds_read_b128 v[190:193], v166 offset:17408
	ds_read_b128 v[194:197], v166 offset:18432
	ds_read_b128 v[198:201], v166 offset:19456
	ds_read_b128 v[202:205], v166 offset:20480
	ds_read_b128 v[206:209], v166 offset:21504
	ds_read_b128 v[210:213], v166 offset:22528
	ds_read_b128 v[214:217], v166 offset:23552
	global_load_lds_dwordx4 v[160:161], off
	s_add_i32 m0, s53, 0x2000
	s_add_u32 s54, s8, 0x40000
	v_lshl_add_u64 v[218:219], s[8:9], 0, v[144:145]
	s_addc_u32 s55, s9, 0
	s_add_i32 s53, s86, s35
	global_load_lds_dwordx4 v[218:219], off
	v_lshl_add_u64 v[220:221], s[54:55], 0, v[140:141]
	s_mov_b32 m0, s53
	v_lshl_add_u64 v[222:223], s[10:11], 0, v[142:143]
	global_load_lds_dwordx4 v[220:221], off
	v_lshl_add_u64 v[220:221], s[54:55], 0, v[144:145]
	s_add_i32 m0, s53, 0x2000
	s_nop 0
	global_load_lds_dwordx4 v[220:221], off
	v_lshl_add_u64 v[220:221], s[10:11], 0, v[138:139]
	s_mov_b32 m0, s67
	s_nop 0
	global_load_lds_dwordx4 v[220:221], off
	s_mov_b32 m0, s68
	s_nop 0
	global_load_lds_dwordx4 v[222:223], off
	s_waitcnt vmcnt(8)
	s_waitcnt lgkmcnt(0)
	s_barrier
; #define PG8_STAGE(bufoff, gbase, voff) do { _Pragma("unroll") for (int _i = 0; _i < 2; ++_i) \
;         __builtin_amdgcn_global_load_lds((const unsigned*)((const char*)(gbase) + (voff)[_i]), (PG8_LAS unsigned*)(lds + (bufoff) + ldsw + _i * 8192), 16, 0, 0); } while (0)
; #define PG8_STAGE_A(bufoff, kbase, h, gv) do { if constexpr (GATHER) { PG8_STAGE(bufoff, kbase, (gv)[h]); } else { PG8_STAGE(bufoff, (kbase) + (h) * hstep, voffA); } } while (0)
; #define PG8_WAIT_V(n) asm volatile("s_waitcnt vmcnt(" #n ")" ::: "memory")
; #define PG8_WAIT_L(n) asm volatile("s_waitcnt lgkmcnt(" #n ")" ::: "memory")
; #define PG8_BAR __builtin_amdgcn_s_barrier()
; #define PG8_SCHED __builtin_amdgcn_sched_barrier(0)
; template <class Epi, class Sched, bool ALIGN_EPI = false, bool SP2 = false, bool FP8 = false, bool GATHER = false>
; __device__ __forceinline__ void gemm_phase(PG8_LAS unsigned char* lds, const Gemm g, const Sched& S, const Epi& E) {
;     ...
;             PG8_WAIT_V(8); PG8_WAIT_L(0); PG8_BAR; PG8_MMA(1, 0, At, B0); PG8_MMA(1, 1, At, B1); PG8_BAR; PG8_SCHED;
;             PG8_LDB(B0, 1, 0); PG8_LDB(B1, 1, 1); PG8_SCHED; PG8_LDA(At, 1, 0); PG8_STAGE_A(PG8_SA(0, 1), a2, 1, gsel);
;             PG8_WAIT_V(8); PG8_WAIT_L(0); PG8_BAR; PG8_MMA(0, 0, At, B0); PG8_MMA(0, 1, At, B1); PG8_BAR; PG8_SCHED;
;             PG8_LDA(At, 1, 1); PG8_STAGE(PG8_SB(1, 0), b3, voffB); PG8_STAGE(PG8_SB(1, 1), b3 + hstep, voffB); PG8_STAGE_A(PG8_SA(1, 0), a3, 0, gsel);
	s_setprio 1
	s_waitcnt lgkmcnt(0)
	v_mfma_f32_16x16x32_bf16 v[102:105], v[74:77], v[186:189], 0
	v_mfma_f32_16x16x32_bf16 v[98:101], v[152:155], v[186:189], 0
	v_mfma_f32_16x16x32_bf16 v[94:97], v[74:77], v[194:197], 0
	v_mfma_f32_16x16x32_bf16 v[90:93], v[152:155], v[194:197], 0
	v_mfma_f32_16x16x32_bf16 v[86:89], v[74:77], v[202:205], 0
	v_mfma_f32_16x16x32_bf16 v[82:85], v[152:155], v[202:205], 0
	v_mfma_f32_16x16x32_bf16 v[70:73], v[74:77], v[210:213], 0
	v_mfma_f32_16x16x32_bf16 v[66:69], v[152:155], v[210:213], 0
	v_mfma_f32_16x16x32_bf16 v[102:105], v[78:81], v[190:193], v[102:105]
	v_mfma_f32_16x16x32_bf16 v[98:101], v[156:159], v[190:193], v[98:101]
	v_mfma_f32_16x16x32_bf16 v[94:97], v[78:81], v[198:201], v[94:97]
	v_mfma_f32_16x16x32_bf16 v[90:93], v[156:159], v[198:201], v[90:93]
	v_mfma_f32_16x16x32_bf16 v[86:89], v[78:81], v[206:209], v[86:89]
	v_mfma_f32_16x16x32_bf16 v[82:85], v[156:159], v[206:209], v[82:85]
	v_mfma_f32_16x16x32_bf16 v[70:73], v[78:81], v[214:217], v[70:73]
	v_mfma_f32_16x16x32_bf16 v[66:69], v[156:159], v[214:217], v[66:69]
	s_setprio 0
	s_setprio 1
	v_mfma_f32_16x16x32_bf16 v[30:33], v[170:173], v[186:189], 0
	v_mfma_f32_16x16x32_bf16 v[26:29], v[178:181], v[186:189], 0
	v_mfma_f32_16x16x32_bf16 v[22:25], v[170:173], v[194:197], 0
	v_mfma_f32_16x16x32_bf16 v[18:21], v[178:181], v[194:197], 0
	v_mfma_f32_16x16x32_bf16 v[14:17], v[170:173], v[202:205], 0
	v_mfma_f32_16x16x32_bf16 v[10:13], v[178:181], v[202:205], 0
	v_mfma_f32_16x16x32_bf16 v[6:9], v[170:173], v[210:213], 0
	v_mfma_f32_16x16x32_bf16 v[2:5], v[178:181], v[210:213], 0
	v_mfma_f32_16x16x32_bf16 v[30:33], v[174:177], v[190:193], v[30:33]
	v_mfma_f32_16x16x32_bf16 v[26:29], v[182:185], v[190:193], v[26:29]
	v_mfma_f32_16x16x32_bf16 v[22:25], v[174:177], v[198:201], v[22:25]
	v_mfma_f32_16x16x32_bf16 v[18:21], v[182:185], v[198:201], v[18:21]
	v_mfma_f32_16x16x32_bf16 v[14:17], v[174:177], v[206:209], v[14:17]
	v_mfma_f32_16x16x32_bf16 v[10:13], v[182:185], v[206:209], v[10:13]
	v_mfma_f32_16x16x32_bf16 v[6:9], v[174:177], v[214:217], v[6:9]
	v_mfma_f32_16x16x32_bf16 v[2:5], v[182:185], v[214:217], v[2:5]
	s_setprio 0
	s_barrier
	s_add_i32 s53, 0, 0x18000
	s_add_i32 s54, 0, 0x1c000
	v_add_u32_e32 v156, s53, v163
	v_add_u32_e32 v182, s54, v163
	ds_read_b128 v[74:77], v156
	ds_read_b128 v[78:81], v156 offset:1024
	ds_read_b128 v[152:155], v156 offset:2048
	ds_read_b128 v[156:159], v156 offset:3072
	ds_read_b128 v[170:173], v182
	ds_read_b128 v[174:177], v182 offset:1024
	ds_read_b128 v[178:181], v182 offset:2048
	ds_read_b128 v[182:185], v182 offset:3072
	s_add_u32 s10, s10, 0x40000
	s_addc_u32 s11, s11, 0
	s_mov_b32 m0, s69
	v_lshl_add_u64 v[224:225], s[10:11], 0, v[138:139]
	ds_read_b128 v[186:189], v166 offset:32768
	ds_read_b128 v[190:193], v166 offset:33792
	ds_read_b128 v[194:197], v166 offset:34816
	ds_read_b128 v[198:201], v166 offset:35840
	ds_read_b128 v[202:205], v166 offset:36864
	ds_read_b128 v[206:209], v166 offset:37888
	ds_read_b128 v[210:213], v166 offset:38912
	ds_read_b128 v[214:217], v166 offset:39936
	global_load_lds_dwordx4 v[224:225], off
	v_lshl_add_u64 v[224:225], s[10:11], 0, v[142:143]
	s_mov_b32 m0, s70
	s_nop 0
	global_load_lds_dwordx4 v[224:225], off
	s_waitcnt vmcnt(8)
	s_waitcnt lgkmcnt(0)
	s_barrier
	s_setprio 1
	s_waitcnt lgkmcnt(0)
	v_mfma_f32_16x16x32_bf16 v[134:137], v[74:77], v[186:189], v[134:137]
	v_mfma_f32_16x16x32_bf16 v[130:133], v[152:155], v[186:189], v[130:133]
	v_mfma_f32_16x16x32_bf16 v[126:129], v[74:77], v[194:197], v[126:129]
	v_mfma_f32_16x16x32_bf16 v[122:125], v[152:155], v[194:197], v[122:125]
	v_mfma_f32_16x16x32_bf16 v[118:121], v[74:77], v[202:205], v[118:121]
	v_mfma_f32_16x16x32_bf16 v[114:117], v[152:155], v[202:205], v[114:117]
	v_mfma_f32_16x16x32_bf16 v[110:113], v[74:77], v[210:213], v[110:113]
	v_mfma_f32_16x16x32_bf16 v[106:109], v[152:155], v[210:213], v[106:109]
	v_mfma_f32_16x16x32_bf16 v[134:137], v[78:81], v[190:193], v[134:137]
	v_mfma_f32_16x16x32_bf16 v[130:133], v[156:159], v[190:193], v[130:133]
	v_mfma_f32_16x16x32_bf16 v[126:129], v[78:81], v[198:201], v[126:129]
	v_mfma_f32_16x16x32_bf16 v[122:125], v[156:159], v[198:201], v[122:125]
	v_mfma_f32_16x16x32_bf16 v[118:121], v[78:81], v[206:209], v[118:121]
	v_mfma_f32_16x16x32_bf16 v[114:117], v[156:159], v[206:209], v[114:117]
	v_mfma_f32_16x16x32_bf16 v[110:113], v[78:81], v[214:217], v[110:113]
	v_mfma_f32_16x16x32_bf16 v[106:109], v[156:159], v[214:217], v[106:109]
	s_setprio 0
	s_setprio 1
	v_mfma_f32_16x16x32_bf16 v[62:65], v[170:173], v[186:189], v[62:65]
	v_mfma_f32_16x16x32_bf16 v[58:61], v[178:181], v[186:189], v[58:61]
	v_mfma_f32_16x16x32_bf16 v[54:57], v[170:173], v[194:197], v[54:57]
	v_mfma_f32_16x16x32_bf16 v[50:53], v[178:181], v[194:197], v[50:53]
	v_mfma_f32_16x16x32_bf16 v[46:49], v[170:173], v[202:205], v[46:49]
	v_mfma_f32_16x16x32_bf16 v[42:45], v[178:181], v[202:205], v[42:45]
	v_mfma_f32_16x16x32_bf16 v[38:41], v[170:173], v[210:213], v[38:41]
	v_mfma_f32_16x16x32_bf16 v[34:37], v[178:181], v[210:213], v[34:37]
	v_mfma_f32_16x16x32_bf16 v[62:65], v[174:177], v[190:193], v[62:65]
	v_mfma_f32_16x16x32_bf16 v[58:61], v[182:185], v[190:193], v[58:61]
	v_mfma_f32_16x16x32_bf16 v[54:57], v[174:177], v[198:201], v[54:57]
	v_mfma_f32_16x16x32_bf16 v[50:53], v[182:185], v[198:201], v[50:53]
	v_mfma_f32_16x16x32_bf16 v[46:49], v[174:177], v[206:209], v[46:49]
	v_mfma_f32_16x16x32_bf16 v[42:45], v[182:185], v[206:209], v[42:45]
	v_mfma_f32_16x16x32_bf16 v[38:41], v[174:177], v[214:217], v[38:41]
	v_mfma_f32_16x16x32_bf16 v[34:37], v[182:185], v[214:217], v[34:37]
	s_setprio 0
	s_barrier
; #define PG8_STAGE(bufoff, gbase, voff) do { _Pragma("unroll") for (int _i = 0; _i < 2; ++_i) \
;         __builtin_amdgcn_global_load_lds((const unsigned*)((const char*)(gbase) + (voff)[_i]), (PG8_LAS unsigned*)(lds + (bufoff) + ldsw + _i * 8192), 16, 0, 0); } while (0)
; #define PG8_STAGE_A(bufoff, kbase, h, gv) do { if constexpr (GATHER) { PG8_STAGE(bufoff, kbase, (gv)[h]); } else { PG8_STAGE(bufoff, (kbase) + (h) * hstep, voffA); } } while (0)
; #define PG8_WAIT_V(n) asm volatile("s_waitcnt vmcnt(" #n ")" ::: "memory")
; #define PG8_WAIT_L(n) asm volatile("s_waitcnt lgkmcnt(" #n ")" ::: "memory")
; #define PG8_BAR __builtin_amdgcn_s_barrier()
; #define PG8_SCHED __builtin_amdgcn_sched_barrier(0)
; template <class Epi, class Sched, bool ALIGN_EPI = false, bool SP2 = false, bool FP8 = false, bool GATHER = false>
; __device__ __forceinline__ void gemm_phase(PG8_LAS unsigned char* lds, const Gemm g, const Sched& S, const Epi& E) {
;     ...
;             PG8_LDA(At, 1, 1); PG8_STAGE(PG8_SB(1, 0), b3, voffB); PG8_STAGE(PG8_SB(1, 1), b3 + hstep, voffB); PG8_STAGE_A(PG8_SA(1, 0), a3, 0, gsel);
;             PG8_WAIT_V(8); PG8_WAIT_L(0); PG8_BAR; PG8_MMA(1, 0, At, B0); PG8_MMA(1, 1, At, B1); PG8_BAR; PG8_SCHED;
	s_add_i32 s10, s53, s35
	v_lshl_add_u64 v[160:161], v[160:161], 0, s[26:27]
	s_mov_b32 m0, s10
	ds_read_b128 v[186:189], v166 offset:49152
	ds_read_b128 v[190:193], v166 offset:50176
	ds_read_b128 v[194:197], v166 offset:51200
	ds_read_b128 v[198:201], v166 offset:52224
	ds_read_b128 v[202:205], v166 offset:53248
	ds_read_b128 v[206:209], v166 offset:54272
	ds_read_b128 v[210:213], v166 offset:55296
	ds_read_b128 v[214:217], v166 offset:56320
	global_load_lds_dwordx4 v[160:161], off
	s_add_i32 m0, s10, 0x2000
	s_add_u32 s8, s8, 0x40080
	v_lshl_add_u64 v[160:161], v[218:219], 0, s[26:27]
	s_addc_u32 s9, s9, 0
	s_add_i32 s10, s54, s35
	global_load_lds_dwordx4 v[160:161], off
	v_lshl_add_u64 v[160:161], s[8:9], 0, v[140:141]
	s_mov_b32 m0, s10
	s_nop 0
	global_load_lds_dwordx4 v[160:161], off
	v_lshl_add_u64 v[160:161], s[8:9], 0, v[144:145]
	s_add_i32 m0, s10, 0x2000
	s_nop 0
	global_load_lds_dwordx4 v[160:161], off
	v_lshl_add_u64 v[160:161], v[220:221], 0, s[26:27]
	s_mov_b32 m0, s77
	s_nop 0
	global_load_lds_dwordx4 v[160:161], off
	v_lshl_add_u64 v[160:161], v[222:223], 0, s[26:27]
	s_mov_b32 m0, s78
	s_nop 0
	global_load_lds_dwordx4 v[160:161], off
	s_waitcnt vmcnt(8)
	s_waitcnt lgkmcnt(0)
	s_barrier
	s_setprio 1
	s_waitcnt lgkmcnt(0)
	v_mfma_f32_16x16x32_bf16 v[102:105], v[74:77], v[186:189], v[102:105]
	v_mfma_f32_16x16x32_bf16 v[98:101], v[152:155], v[186:189], v[98:101]
	v_mfma_f32_16x16x32_bf16 v[94:97], v[74:77], v[194:197], v[94:97]
	v_mfma_f32_16x16x32_bf16 v[90:93], v[152:155], v[194:197], v[90:93]
	v_mfma_f32_16x16x32_bf16 v[86:89], v[74:77], v[202:205], v[86:89]
	v_mfma_f32_16x16x32_bf16 v[82:85], v[152:155], v[202:205], v[82:85]
	v_mfma_f32_16x16x32_bf16 v[70:73], v[74:77], v[210:213], v[70:73]
	v_mfma_f32_16x16x32_bf16 v[66:69], v[152:155], v[210:213], v[66:69]
	v_mfma_f32_16x16x32_bf16 v[102:105], v[78:81], v[190:193], v[102:105]
	v_mfma_f32_16x16x32_bf16 v[98:101], v[156:159], v[190:193], v[98:101]
	v_mfma_f32_16x16x32_bf16 v[94:97], v[78:81], v[198:201], v[94:97]
	v_mfma_f32_16x16x32_bf16 v[90:93], v[156:159], v[198:201], v[90:93]
	v_mfma_f32_16x16x32_bf16 v[86:89], v[78:81], v[206:209], v[86:89]
	v_mfma_f32_16x16x32_bf16 v[82:85], v[156:159], v[206:209], v[82:85]
	v_mfma_f32_16x16x32_bf16 v[70:73], v[78:81], v[214:217], v[70:73]
	v_mfma_f32_16x16x32_bf16 v[66:69], v[156:159], v[214:217], v[66:69]
	s_setprio 0
	s_setprio 1
	v_mfma_f32_16x16x32_bf16 v[30:33], v[170:173], v[186:189], v[30:33]
	v_mfma_f32_16x16x32_bf16 v[26:29], v[178:181], v[186:189], v[26:29]
	v_mfma_f32_16x16x32_bf16 v[22:25], v[170:173], v[194:197], v[22:25]
	v_mfma_f32_16x16x32_bf16 v[18:21], v[178:181], v[194:197], v[18:21]
	v_mfma_f32_16x16x32_bf16 v[14:17], v[170:173], v[202:205], v[14:17]
	v_mfma_f32_16x16x32_bf16 v[10:13], v[178:181], v[202:205], v[10:13]
	v_mfma_f32_16x16x32_bf16 v[6:9], v[170:173], v[210:213], v[6:9]
	v_mfma_f32_16x16x32_bf16 v[2:5], v[178:181], v[210:213], v[2:5]
	v_mfma_f32_16x16x32_bf16 v[30:33], v[174:177], v[190:193], v[30:33]
	v_mfma_f32_16x16x32_bf16 v[26:29], v[182:185], v[190:193], v[26:29]
	v_mfma_f32_16x16x32_bf16 v[22:25], v[174:177], v[198:201], v[22:25]
	v_mfma_f32_16x16x32_bf16 v[18:21], v[182:185], v[198:201], v[18:21]
	v_mfma_f32_16x16x32_bf16 v[14:17], v[174:177], v[206:209], v[14:17]
	v_mfma_f32_16x16x32_bf16 v[10:13], v[182:185], v[206:209], v[10:13]
	v_mfma_f32_16x16x32_bf16 v[6:9], v[174:177], v[214:217], v[6:9]
	v_mfma_f32_16x16x32_bf16 v[2:5], v[182:185], v[214:217], v[2:5]
	s_setprio 0
	s_barrier
	s_add_i32 s45, s45, 2
	s_add_u32 s6, s6, 0x100
	s_addc_u32 s7, s7, 0
	s_add_u32 s15, s15, 0x100
	s_addc_u32 s16, s16, 0
	s_cmp_gt_u32 s45, 13

;     __device__ __forceinline__ int brow(const pg8::Unit& u) const { return (u.pn >> 8) * Nper + (u.pn & 255) * 256; }
; template <class Epi, class Sched, bool ALIGN_EPI = false, bool SP2 = false, bool FP8 = false, bool GATHER = false>
; __device__ __forceinline__ void gemm_phase(PG8_LAS unsigned char* lds, const Gemm g, const Sched& S, const Epi& E) {
;     ...
;         const bool has_next = S.next(ui + 1, nxt);
;         const char* nA = (has_next && !GATHER) ? (const char*)g.A + (size_t)nxt.pm * tstep : cA; const char* nB = has_next ? (const char*)g.Bt + (size_t)S.brow(nxt) * (size_t)K * 2 : cB;
; #pragma nounroll
;         for (int t = 0; t < nt; t += 2) {
;             const bool last = (t == nt - 2);
;             const char* a1 = cA + (size_t)(t + 1) * kstep;
;             const char* a2 = last ? nA : cA + (size_t)(t + 2) * kstep; const char* b2 = last ? nB : cB + (size_t)(t + 2) * kstep;
;             const char* a3 = a2 + kstep; const char* b3 = b2 + kstep;
;             if (last && has_next) S.a_ready(nxt);
;             if (last) E.pre(cur, wid, lane);
;             if constexpr (GATHER) { if (t == nt - 4 && has_next) { _Pragma("unroll") for (int h_ = 0; h_ < 2; ++h_) _Pragma("unroll") for (int i_ = 0; i_ < 2; ++i_)
;                 asm volatile("global_load_dword %0, %1, off" : "+v"(graw[h_][i_]) : "v"(S.rowtok + (nxt.pm * BM + h_ * HALF + gR[i_])) : "memory"); } }
;             unsigned gsel[2][2];
;             if constexpr (GATHER) { _Pragma("unroll") for (int h_ = 0; h_ < 2; ++h_) _Pragma("unroll") for (int i_ = 0; i_ < 2; ++i_) { if (last && has_next) gnxt[h_][i_] = graw[h_][i_] * (unsigned)(K * 2) + gC[i_]; gsel[h_][i_] = (last && has_next) ? gnxt[h_][i_] : gcur[h_][i_]; } }
;     __device__ __forceinline__ void pre(const pg8::Unit& u, int wid, int lane) const {
;         if (wid == 0) lds_dma16(bias + (size_t)(u.pn >> 8) * 2048 + (lane >> 5) * 1024 + (u.pn & 255) * 128 + (lane & 31) * 4, (unsigned)(uintptr_t)(lds + LDS_EPI)); }
.LBB0_877:
	s_ashr_i32 s52, s50, 8
	s_ashr_i32 s53, s52, 31
	s_lshl_b32 s22, s50, 7
	s_lshl_b64 s[52:53], s[52:53], 13
	s_and_b32 s83, s22, 0x7f80
	s_lshl_b32 s50, s80, 8
	v_lshl_add_u64 v[6:7], v[172:173], 0, s[52:53]
	s_lshl_b32 s22, s83, 2
	v_lshl_add_u64 v[6:7], v[6:7], 0, s[22:23]
	s_ashr_i32 s51, s50, 31
	v_lshl_add_u64 v[182:183], v[6:7], 0, v[174:175]
	v_lshl_add_u64 v[6:7], s[50:51], 0, v[164:165]
	v_lshl_add_u64 v[6:7], v[6:7], 2, s[12:13]
	v_add_u32_e32 v2, s50, v162
	v_add_u32_e32 v4, s50, v164
	v_lshl_add_u64 v[184:185], v[6:7], 0, s[28:29]
	v_lshl_add_u64 v[6:7], s[50:51], 0, v[162:163]
	v_ashrrev_i32_e32 v3, 31, v2
	v_ashrrev_i32_e32 v5, 31, v4
	v_mov_b32_e32 v179, v171
	v_mov_b32_e32 v177, v171
	v_lshl_add_u64 v[6:7], v[6:7], 2, s[12:13]
	s_add_u32 s22, s48, 0x100
	v_lshl_add_u64 v[186:187], v[6:7], 0, s[28:29]
	v_lshl_add_u64 v[188:189], v[4:5], 2, s[12:13]
	v_lshl_add_u64 v[190:191], v[2:3], 2, s[12:13]
	v_lshl_add_u64 v[192:193], s[20:21], 0, v[176:177]
	v_lshl_add_u64 v[194:195], s[20:21], 0, v[178:179]
	s_addc_u32 s84, s49, 0
	s_mov_b32 s85, -2
	s_mov_b64 s[48:49], 0
	s_xor_b64 s[50:51], s[46:47], -1

; #define PG8_STAGE(bufoff, gbase, voff) do { _Pragma("unroll") for (int _i = 0; _i < 2; ++_i) \
;         __builtin_amdgcn_global_load_lds((const unsigned*)((const char*)(gbase) + (voff)[_i]), (PG8_LAS unsigned*)(lds + (bufoff) + ldsw + _i * 8192), 16, 0, 0); } while (0)
; #define PG8_STAGE_A(bufoff, kbase, h, gv) do { if constexpr (GATHER) { PG8_STAGE(bufoff, kbase, (gv)[h]); } else { PG8_STAGE(bufoff, (kbase) + (h) * hstep, voffA); } } while (0)
; #define PG8_WAIT_V(n) asm volatile("s_waitcnt vmcnt(" #n ")" ::: "memory")
; #define PG8_WAIT_L(n) asm volatile("s_waitcnt lgkmcnt(" #n ")" ::: "memory")
; #define PG8_BAR __builtin_amdgcn_s_barrier()
; #define PG8_SCHED __builtin_amdgcn_sched_barrier(0)
; template <class Epi, class Sched, bool ALIGN_EPI = false, bool SP2 = false, bool FP8 = false, bool GATHER = false>
; __device__ __forceinline__ void gemm_phase(PG8_LAS unsigned char* lds, const Gemm g, const Sched& S, const Epi& E) {
;     ...
;             if constexpr (GATHER) { _Pragma("unroll") for (int h_ = 0; h_ < 2; ++h_) _Pragma("unroll") for (int i_ = 0; i_ < 2; ++i_) { if (last && has_next) gnxt[h_][i_] = graw[h_][i_] * (unsigned)(K * 2) + gC[i_]; gsel[h_][i_] = (last && has_next) ? gnxt[h_][i_] : gcur[h_][i_]; } }
;             if constexpr (SP2) {
;             PG8_LDB(B0, 0, 0); PG8_LDB(B1, 0, 1); PG8_SCHED; PG8_LDA(At, 0, 0); PG8_STAGE_A(PG8_SA(1, 1), a1, 1, gcur);
;             PG8_WAIT_V(8); PG8_WAIT_L(0); PG8_BAR; PG8_MMA(0, 0, At, B0); PG8_MMA(0, 1, At, B1); PG8_BAR; PG8_SCHED;
;             PG8_LDA(At, 0, 1); PG8_STAGE(PG8_SB(0, 0), b2, voffB); PG8_STAGE(PG8_SB(0, 1), b2 + hstep, voffB); PG8_STAGE_A(PG8_SA(0, 0), a2, 0, gsel);
;             PG8_WAIT_V(8); PG8_WAIT_L(0); PG8_BAR; PG8_MMA(1, 0, At, B0); PG8_MMA(1, 1, At, B1); PG8_BAR; PG8_SCHED;
.Lpeel878_body:
	s_add_u32 s52, s8, s48
	s_addc_u32 s53, s9, s49
	s_add_u32 s54, s52, 0x19200100
	s_addc_u32 s55, s53, 0
	s_and_b64 s[52:53], s[56:57], exec
	s_cselect_b32 s55, s11, s55
	s_cselect_b32 s54, s10, s54
	s_add_u32 s86, s22, s48
	s_addc_u32 s87, s84, s49
	s_and_b64 s[52:53], s[56:57], exec
	s_cselect_b32 s53, s45, s87
	s_cselect_b32 s52, s44, s86
	v_lshl_add_u32 v2, v213, 10, v1
	s_and_b64 vcc, s[46:47], s[56:57]
	v_cndmask_b32_e32 v209, v209, v2, vcc
	v_cndmask_b32_e32 v170, v217, v2, vcc
	v_lshl_add_u32 v2, v214, 10, v204
	v_cndmask_b32_e32 v210, v210, v2, vcc
	v_cndmask_b32_e32 v200, v180, v2, vcc
	v_add_u32_e32 v2, s76, v206
	v_add_u32_e32 v14, s77, v206
	ds_read_b128 v[18:21], v2
	ds_read_b128 v[22:25], v2 offset:1024
	ds_read_b128 v[26:29], v2 offset:2048
	ds_read_b128 v[30:33], v2 offset:3072
	ds_read_b128 v[2:5], v14
	ds_read_b128 v[6:9], v14 offset:1024
	ds_read_b128 v[10:13], v14 offset:2048
	ds_read_b128 v[14:17], v14 offset:3072
	v_lshl_add_u32 v177, v215, 10, v1
	v_lshl_add_u32 v179, v216, 10, v204
	v_cndmask_b32_e32 v211, v211, v177, vcc
	v_cndmask_b32_e32 v212, v212, v179, vcc
	v_cndmask_b32_e32 v177, v178, v177, vcc
	v_cndmask_b32_e32 v179, v176, v179, vcc
	v_lshl_add_u64 v[196:197], v[194:195], 0, s[48:49]
	s_add_i32 m0, s63, 0xc000
	ds_read_b128 v[218:221], v207
	ds_read_b128 v[222:225], v207 offset:1024
	ds_read_b128 v[226:229], v207 offset:2048
	ds_read_b128 v[230:233], v207 offset:3072
	ds_read_b128 v[234:237], v207 offset:4096
	ds_read_b128 v[238:241], v207 offset:5120
	ds_read_b128 v[242:245], v207 offset:6144
	ds_read_b128 v[246:249], v207 offset:7168
	global_load_lds_dwordx4 v[196:197], off
	v_lshl_add_u64 v[196:197], v[192:193], 0, s[48:49]
	s_add_i32 m0, s63, 0xe000
	s_nop 0
	global_load_lds_dwordx4 v[196:197], off
	s_waitcnt vmcnt(8)
	s_waitcnt lgkmcnt(0)
	s_barrier
	s_setprio 1
	s_waitcnt lgkmcnt(0)
	v_mfma_f32_16x16x128_f8f6f4 v[158:161], v[18:25], v[218:225], 0
	v_mfma_f32_16x16x128_f8f6f4 v[150:153], v[26:33], v[218:225], 0
	v_mfma_f32_16x16x128_f8f6f4 v[142:145], v[18:25], v[226:233], 0
	v_mfma_f32_16x16x128_f8f6f4 v[134:137], v[26:33], v[226:233], 0
	v_mfma_f32_16x16x128_f8f6f4 v[126:129], v[18:25], v[234:241], 0
	v_mfma_f32_16x16x128_f8f6f4 v[118:121], v[26:33], v[234:241], 0
	v_mfma_f32_16x16x128_f8f6f4 v[110:113], v[18:25], v[242:249], 0
	v_mfma_f32_16x16x128_f8f6f4 v[102:105], v[26:33], v[242:249], 0
	s_setprio 0
	s_setprio 1
	v_mfma_f32_16x16x128_f8f6f4 v[154:157], v[2:9], v[218:225], 0
	v_mfma_f32_16x16x128_f8f6f4 v[146:149], v[10:17], v[218:225], 0
	v_mfma_f32_16x16x128_f8f6f4 v[138:141], v[2:9], v[226:233], 0
	v_mfma_f32_16x16x128_f8f6f4 v[130:133], v[10:17], v[226:233], 0
	v_mfma_f32_16x16x128_f8f6f4 v[122:125], v[2:9], v[234:241], 0
	v_mfma_f32_16x16x128_f8f6f4 v[114:117], v[10:17], v[234:241], 0
	v_mfma_f32_16x16x128_f8f6f4 v[106:109], v[2:9], v[242:249], 0
	v_mfma_f32_16x16x128_f8f6f4 v[98:101], v[10:17], v[242:249], 0
	s_setprio 0
	s_barrier
	s_add_i32 s56, s76, s60
	v_lshl_add_u64 v[196:197], s[52:53], 0, v[168:169]
	s_mov_b32 m0, s56
	ds_read_b128 v[218:221], v207 offset:16384
	ds_read_b128 v[222:225], v207 offset:17408
	ds_read_b128 v[226:229], v207 offset:18432
	ds_read_b128 v[230:233], v207 offset:19456
	ds_read_b128 v[234:237], v207 offset:20480
	ds_read_b128 v[238:241], v207 offset:21504
	ds_read_b128 v[242:245], v207 offset:22528
	ds_read_b128 v[246:249], v207 offset:23552
	global_load_lds_dwordx4 v[196:197], off
	s_add_i32 m0, s56, 0x2000
	s_add_u32 s56, s52, 0x20000
	v_lshl_add_u64 v[198:199], s[52:53], 0, v[166:167]
	s_addc_u32 s57, s53, 0
	s_add_i32 s86, s77, s60
	global_load_lds_dwordx4 v[198:199], off
	v_lshl_add_u64 v[202:203], s[56:57], 0, v[168:169]
	s_mov_b32 m0, s86
	v_mov_b32_e32 v201, v171
	global_load_lds_dwordx4 v[202:203], off
	v_lshl_add_u64 v[202:203], s[56:57], 0, v[166:167]
	s_add_i32 m0, s86, 0x2000
	s_nop 0
	global_load_lds_dwordx4 v[202:203], off
	s_mov_b32 m0, s63
	v_lshl_add_u64 v[202:203], s[54:55], 0, v[170:171]
	global_load_lds_dwordx4 v170, s[54:55]
	s_mov_b32 m0, s65
	s_nop 0
	global_load_lds_dwordx4 v200, s[54:55]
	s_waitcnt vmcnt(8)
	s_waitcnt lgkmcnt(0)
	v_lshl_add_u64 v[200:201], s[54:55], 0, v[200:201]
	s_barrier
	s_setprio 1
	s_waitcnt lgkmcnt(0)
	v_mfma_f32_16x16x128_f8f6f4 v[94:97], v[18:25], v[218:225], 0
	v_mfma_f32_16x16x128_f8f6f4 v[86:89], v[26:33], v[218:225], 0
	v_mfma_f32_16x16x128_f8f6f4 v[78:81], v[18:25], v[226:233], 0
	v_mfma_f32_16x16x128_f8f6f4 v[70:73], v[26:33], v[226:233], 0
	v_mfma_f32_16x16x128_f8f6f4 v[62:65], v[18:25], v[234:241], 0
	v_mfma_f32_16x16x128_f8f6f4 v[54:57], v[26:33], v[234:241], 0
	v_mfma_f32_16x16x128_f8f6f4 v[46:49], v[18:25], v[242:249], 0
	v_mfma_f32_16x16x128_f8f6f4 v[38:41], v[26:33], v[242:249], 0
	s_setprio 0
	s_setprio 1
	v_mfma_f32_16x16x128_f8f6f4 v[90:93], v[2:9], v[218:225], 0
	v_mfma_f32_16x16x128_f8f6f4 v[82:85], v[10:17], v[218:225], 0
	v_mfma_f32_16x16x128_f8f6f4 v[74:77], v[2:9], v[226:233], 0
	v_mfma_f32_16x16x128_f8f6f4 v[66:69], v[10:17], v[226:233], 0
	v_mfma_f32_16x16x128_f8f6f4 v[58:61], v[2:9], v[234:241], 0
	v_mfma_f32_16x16x128_f8f6f4 v[50:53], v[10:17], v[234:241], 0
	v_mfma_f32_16x16x128_f8f6f4 v[42:45], v[2:9], v[242:249], 0
	v_mfma_f32_16x16x128_f8f6f4 v[34:37], v[10:17], v[242:249], 0
	s_setprio 0
	s_barrier
; #define PG8_STAGE(bufoff, gbase, voff) do { _Pragma("unroll") for (int _i = 0; _i < 2; ++_i) \
;         __builtin_amdgcn_global_load_lds((const unsigned*)((const char*)(gbase) + (voff)[_i]), (PG8_LAS unsigned*)(lds + (bufoff) + ldsw + _i * 8192), 16, 0, 0); } while (0)
; #define PG8_STAGE_A(bufoff, kbase, h, gv) do { if constexpr (GATHER) { PG8_STAGE(bufoff, kbase, (gv)[h]); } else { PG8_STAGE(bufoff, (kbase) + (h) * hstep, voffA); } } while (0)
; #define PG8_WAIT_V(n) asm volatile("s_waitcnt vmcnt(" #n ")" ::: "memory")
; #define PG8_WAIT_L(n) asm volatile("s_waitcnt lgkmcnt(" #n ")" ::: "memory")
; #define PG8_BAR __builtin_amdgcn_s_barrier()
; #define PG8_SCHED __builtin_amdgcn_sched_barrier(0)
; template <class Epi, class Sched, bool ALIGN_EPI = false, bool SP2 = false, bool FP8 = false, bool GATHER = false>
; __device__ __forceinline__ void gemm_phase(PG8_LAS unsigned char* lds, const Gemm g, const Sched& S, const Epi& E) {
;     ...
;             PG8_LDB(B0, 1, 0); PG8_LDB(B1, 1, 1); PG8_SCHED; PG8_LDA(At, 1, 0); PG8_STAGE_A(PG8_SA(0, 1), a2, 1, gsel);
;             PG8_WAIT_V(8); PG8_WAIT_L(0); PG8_BAR; PG8_MMA(0, 0, At, B0); PG8_MMA(0, 1, At, B1); PG8_BAR; PG8_SCHED;
;             PG8_LDA(At, 1, 1); PG8_STAGE(PG8_SB(1, 0), b3, voffB); PG8_STAGE(PG8_SB(1, 1), b3 + hstep, voffB); PG8_STAGE_A(PG8_SA(1, 0), a3, 0, gsel);
;             PG8_WAIT_V(8); PG8_WAIT_L(0); PG8_BAR; PG8_MMA(1, 0, At, B0); PG8_MMA(1, 1, At, B1); PG8_BAR; PG8_SCHED;
	s_add_i32 s56, 0, 0x18000
	s_add_i32 s57, 0, 0x1c000
	v_add_u32_e32 v14, s56, v206
	v_add_u32_e32 v30, s57, v206
	ds_read_b128 v[2:5], v14
	ds_read_b128 v[6:9], v14 offset:1024
	ds_read_b128 v[10:13], v14 offset:2048
	ds_read_b128 v[14:17], v14 offset:3072
	ds_read_b128 v[18:21], v30
	ds_read_b128 v[22:25], v30 offset:1024
	ds_read_b128 v[26:29], v30 offset:2048
	ds_read_b128 v[30:33], v30 offset:3072
	s_mov_b32 m0, s66
	ds_read_b128 v[218:221], v207 offset:32768
	ds_read_b128 v[222:225], v207 offset:33792
	ds_read_b128 v[226:229], v207 offset:34816
	ds_read_b128 v[230:233], v207 offset:35840
	ds_read_b128 v[234:237], v207 offset:36864
	ds_read_b128 v[238:241], v207 offset:37888
	ds_read_b128 v[242:245], v207 offset:38912
	ds_read_b128 v[246:249], v207 offset:39936
	global_load_lds_dwordx4 v177, s[54:55]
	s_mov_b32 m0, s67
	s_nop 0
	global_load_lds_dwordx4 v179, s[54:55]
	s_waitcnt vmcnt(8)
	s_waitcnt lgkmcnt(0)
	s_barrier
	s_setprio 1
	s_waitcnt lgkmcnt(0)
	v_mfma_f32_16x16x128_f8f6f4 v[158:161], v[2:9], v[218:225], v[158:161]
	v_mfma_f32_16x16x128_f8f6f4 v[150:153], v[10:17], v[218:225], v[150:153]
	v_mfma_f32_16x16x128_f8f6f4 v[142:145], v[2:9], v[226:233], v[142:145]
	v_mfma_f32_16x16x128_f8f6f4 v[134:137], v[10:17], v[226:233], v[134:137]
	v_mfma_f32_16x16x128_f8f6f4 v[126:129], v[2:9], v[234:241], v[126:129]
	v_mfma_f32_16x16x128_f8f6f4 v[118:121], v[10:17], v[234:241], v[118:121]
	v_mfma_f32_16x16x128_f8f6f4 v[110:113], v[2:9], v[242:249], v[110:113]
	v_mfma_f32_16x16x128_f8f6f4 v[102:105], v[10:17], v[242:249], v[102:105]
	s_setprio 0
	s_setprio 1
	v_mfma_f32_16x16x128_f8f6f4 v[154:157], v[18:25], v[218:225], v[154:157]
	v_mfma_f32_16x16x128_f8f6f4 v[146:149], v[26:33], v[218:225], v[146:149]
	v_mfma_f32_16x16x128_f8f6f4 v[138:141], v[18:25], v[226:233], v[138:141]
	v_mfma_f32_16x16x128_f8f6f4 v[130:133], v[26:33], v[226:233], v[130:133]
	v_mfma_f32_16x16x128_f8f6f4 v[122:125], v[18:25], v[234:241], v[122:125]
	v_mfma_f32_16x16x128_f8f6f4 v[114:117], v[26:33], v[234:241], v[114:117]
	v_mfma_f32_16x16x128_f8f6f4 v[106:109], v[18:25], v[242:249], v[106:109]
	v_mfma_f32_16x16x128_f8f6f4 v[98:101], v[26:33], v[242:249], v[98:101]
	s_setprio 0
	s_barrier
	s_add_i32 s54, s56, s60
	v_lshl_add_u64 v[196:197], v[196:197], 0, s[18:19]
	s_mov_b32 m0, s54
	ds_read_b128 v[218:221], v207 offset:49152
	ds_read_b128 v[222:225], v207 offset:50176
	ds_read_b128 v[226:229], v207 offset:51200
	ds_read_b128 v[230:233], v207 offset:52224
	ds_read_b128 v[234:237], v207 offset:53248
	ds_read_b128 v[238:241], v207 offset:54272
	ds_read_b128 v[242:245], v207 offset:55296
	ds_read_b128 v[246:249], v207 offset:56320
	global_load_lds_dwordx4 v[196:197], off
	s_add_i32 m0, s54, 0x2000
	s_add_u32 s52, s52, 0x20080
	v_lshl_add_u64 v[196:197], v[198:199], 0, s[18:19]
	s_addc_u32 s53, s53, 0
	s_add_i32 s54, s57, s60
	global_load_lds_dwordx4 v[196:197], off
	v_lshl_add_u64 v[196:197], s[52:53], 0, v[168:169]
	s_mov_b32 m0, s54
	s_nop 0
	global_load_lds_dwordx4 v[196:197], off
	v_lshl_add_u64 v[196:197], s[52:53], 0, v[166:167]
	s_add_i32 m0, s54, 0x2000
	s_nop 0
	global_load_lds_dwordx4 v[196:197], off
	v_lshl_add_u64 v[196:197], v[202:203], 0, s[18:19]
	s_mov_b32 m0, s70
	s_nop 0
	global_load_lds_dwordx4 v[196:197], off
	v_lshl_add_u64 v[196:197], v[200:201], 0, s[18:19]
	s_mov_b32 m0, s71
	s_nop 0
	global_load_lds_dwordx4 v[196:197], off
	s_waitcnt vmcnt(8)
	s_waitcnt lgkmcnt(0)
	s_barrier
	s_setprio 1
	s_waitcnt lgkmcnt(0)
	v_mfma_f32_16x16x128_f8f6f4 v[94:97], v[2:9], v[218:225], v[94:97]
	v_mfma_f32_16x16x128_f8f6f4 v[86:89], v[10:17], v[218:225], v[86:89]
	v_mfma_f32_16x16x128_f8f6f4 v[78:81], v[2:9], v[226:233], v[78:81]
	v_mfma_f32_16x16x128_f8f6f4 v[70:73], v[10:17], v[226:233], v[70:73]
	v_mfma_f32_16x16x128_f8f6f4 v[62:65], v[2:9], v[234:241], v[62:65]
	v_mfma_f32_16x16x128_f8f6f4 v[54:57], v[10:17], v[234:241], v[54:57]
	v_mfma_f32_16x16x128_f8f6f4 v[46:49], v[2:9], v[242:249], v[46:49]
	v_mfma_f32_16x16x128_f8f6f4 v[38:41], v[10:17], v[242:249], v[38:41]
	s_setprio 0
	s_setprio 1
	v_mfma_f32_16x16x128_f8f6f4 v[90:93], v[18:25], v[218:225], v[90:93]
	v_mfma_f32_16x16x128_f8f6f4 v[82:85], v[26:33], v[218:225], v[82:85]
	v_mfma_f32_16x16x128_f8f6f4 v[74:77], v[18:25], v[226:233], v[74:77]
	v_mfma_f32_16x16x128_f8f6f4 v[66:69], v[26:33], v[226:233], v[66:69]
	v_mfma_f32_16x16x128_f8f6f4 v[58:61], v[18:25], v[234:241], v[58:61]
	v_mfma_f32_16x16x128_f8f6f4 v[50:53], v[26:33], v[234:241], v[50:53]
	v_mfma_f32_16x16x128_f8f6f4 v[42:45], v[18:25], v[242:249], v[42:45]
	v_mfma_f32_16x16x128_f8f6f4 v[34:37], v[26:33], v[242:249], v[34:37]
	s_setprio 0
	s_barrier
	s_add_i32 s85, s85, 2
	s_add_u32 s48, s48, 0x100
	s_addc_u32 s49, s49, 0
	s_cmp_gt_u32 s85, 5
	s_cbranch_scc1 .LBB0_883
	s_branch .LBB0_879

;     __device__ __forceinline__ int brow(const pg8::Unit& u) const { return (u.pn >> 8) * Nper + (u.pn & 255) * 256; }
; template <class Epi, class Sched, bool ALIGN_EPI = false, bool SP2 = false, bool FP8 = false, bool GATHER = false>
; __device__ __forceinline__ void gemm_phase(PG8_LAS unsigned char* lds, const Gemm g, const Sched& S, const Epi& E) {
;     ...
;         const bool has_next = S.next(ui + 1, nxt);
;         const char* nA = (has_next && !GATHER) ? (const char*)g.A + (size_t)nxt.pm * tstep : cA; const char* nB = has_next ? (const char*)g.Bt + (size_t)S.brow(nxt) * (size_t)K * 2 : cB;
; #pragma nounroll
;         for (int t = 0; t < nt; t += 2) {
;             const bool last = (t == nt - 2);
;             const char* a1 = cA + (size_t)(t + 1) * kstep;
;             const char* a2 = last ? nA : cA + (size_t)(t + 2) * kstep; const char* b2 = last ? nB : cB + (size_t)(t + 2) * kstep;
;     ...
;         for (int a = 0; a < 2; ++a)
; #pragma unroll
;             for (int b = 0; b < 2; ++b)
; #pragma unroll
;                 for (int m = 0; m < 4; ++m)
; #pragma unroll
;                     for (int n = 0; n < 2; ++n) acc[a][b][m][n] = (f32x4){0.f, 0.f, 0.f, 0.f};
;         cur = nxt; cA = nA; cB = nB; ++ui;
.LBB0_952:
	s_ashr_i32 s31, s30, 31
	s_lshl_b64 s[34:35], s[30:31], 18
	s_add_u32 s34, s57, s34
	s_addc_u32 s35, s58, s35
	s_and_b64 s[80:81], s[44:45], exec
	s_cselect_b32 s80, s35, s49
	s_cselect_b32 s81, s34, s48
	s_ashr_i32 s84, s52, 8
	s_ashr_i32 s47, s46, 31
	s_ashr_i32 s85, s84, 31
	s_lshl_b32 s31, s52, 8
	s_lshl_b64 s[82:83], s[46:47], 10
	s_lshl_b64 s[84:85], s[84:85], 12
	s_and_b32 s31, s31, 0xff00
	s_add_u32 s47, s10, s84
	s_addc_u32 s53, s11, s85
	s_lshl_b32 s52, s31, 2
	s_add_u32 s52, s47, s52
	s_addc_u32 s53, s53, 0
	s_add_u32 s48, s48, 0x20080
	s_addc_u32 s49, s49, 0
	s_add_u32 s47, s50, 0x100
	v_lshl_add_u64 v[178:179], v[170:171], 0, s[82:83]
	v_lshl_add_u64 v[180:181], s[52:53], 0, v[176:177]
	s_addc_u32 s82, s51, 0
	s_mov_b32 s83, -2

; #define PG8_STAGE(bufoff, gbase, voff) do { _Pragma("unroll") for (int _i = 0; _i < 2; ++_i) \
;         __builtin_amdgcn_global_load_lds((const unsigned*)((const char*)(gbase) + (voff)[_i]), (PG8_LAS unsigned*)(lds + (bufoff) + ldsw + _i * 8192), 16, 0, 0); } while (0)
; #define PG8_STAGE_A(bufoff, kbase, h, gv) do { if constexpr (GATHER) { PG8_STAGE(bufoff, kbase, (gv)[h]); } else { PG8_STAGE(bufoff, (kbase) + (h) * hstep, voffA); } } while (0)
; #define PG8_WAIT_V(n) asm volatile("s_waitcnt vmcnt(" #n ")" ::: "memory")
; #define PG8_WAIT_L(n) asm volatile("s_waitcnt lgkmcnt(" #n ")" ::: "memory")
; #define PG8_BAR __builtin_amdgcn_s_barrier()
; #define PG8_SCHED __builtin_amdgcn_sched_barrier(0)
; template <class Epi, class Sched, bool ALIGN_EPI = false, bool SP2 = false, bool FP8 = false, bool GATHER = false>
; __device__ __forceinline__ void gemm_phase(PG8_LAS unsigned char* lds, const Gemm g, const Sched& S, const Epi& E) {
;     ...
;             PG8_LDB(B0, 0, 0); PG8_LDB(B1, 0, 1); PG8_SCHED; PG8_LDA(At, 0, 0); PG8_STAGE_A(PG8_SA(1, 1), a1, 1, gcur);
;             PG8_WAIT_V(8); PG8_WAIT_L(0); PG8_BAR; PG8_MMA(0, 0, At, B0); PG8_MMA(0, 1, At, B1); PG8_BAR; PG8_SCHED;
;             PG8_LDA(At, 0, 1); PG8_STAGE(PG8_SB(0, 0), b2, voffB); PG8_STAGE(PG8_SB(0, 1), b2 + hstep, voffB); PG8_STAGE_A(PG8_SA(0, 0), a2, 0, gsel);
;             PG8_WAIT_V(8); PG8_WAIT_L(0); PG8_BAR; PG8_MMA(1, 0, At, B0); PG8_MMA(1, 1, At, B1); PG8_BAR; PG8_SCHED;
.Lpeel953_body:
	v_add_u32_e32 v2, s76, v191
	v_add_u32_e32 v14, s77, v191
	ds_read_b128 v[18:21], v2
	ds_read_b128 v[22:25], v2 offset:1024
	ds_read_b128 v[26:29], v2 offset:2048
	ds_read_b128 v[30:33], v2 offset:3072
	ds_read_b128 v[2:5], v14
	ds_read_b128 v[6:9], v14 offset:1024
	ds_read_b128 v[10:13], v14 offset:2048
	ds_read_b128 v[14:17], v14 offset:3072
	s_add_u32 s52, s48, 0xfffe0080
	s_addc_u32 s53, s49, -1
	s_and_b64 s[50:51], s[50:51], exec
	s_cselect_b32 s53, s80, s53
	s_cselect_b32 s52, s81, s52
	s_cselect_b32 s51, s29, s82
	s_cselect_b32 s50, s28, s47
	v_lshl_add_u64 v[218:219], s[48:49], 0, v[172:173]
	s_add_i32 m0, s62, 0xc000
	ds_read_b128 v[182:185], v192
	ds_read_b128 v[186:189], v192 offset:1024
	ds_read_b128 v[194:197], v192 offset:2048
	ds_read_b128 v[198:201], v192 offset:3072
	ds_read_b128 v[202:205], v192 offset:4096
	ds_read_b128 v[206:209], v192 offset:5120
	ds_read_b128 v[210:213], v192 offset:6144
	ds_read_b128 v[214:217], v192 offset:7168
	global_load_lds_dwordx4 v[218:219], off
	v_lshl_add_u64 v[218:219], s[48:49], 0, v[174:175]
	s_add_i32 m0, s62, 0xe000
	s_nop 0
	global_load_lds_dwordx4 v[218:219], off
	s_waitcnt vmcnt(8)
	s_waitcnt lgkmcnt(0)
	s_barrier
	s_setprio 1
	s_waitcnt lgkmcnt(0)
	v_mfma_f32_16x16x128_f8f6f4 v[158:161], v[18:25], v[182:189], 0
	v_mfma_f32_16x16x128_f8f6f4 v[154:157], v[26:33], v[182:189], 0
	v_mfma_f32_16x16x128_f8f6f4 v[150:153], v[18:25], v[194:201], 0
	v_mfma_f32_16x16x128_f8f6f4 v[146:149], v[26:33], v[194:201], 0
	v_mfma_f32_16x16x128_f8f6f4 v[130:133], v[18:25], v[202:209], 0
	v_mfma_f32_16x16x128_f8f6f4 v[122:125], v[26:33], v[202:209], 0
	v_mfma_f32_16x16x128_f8f6f4 v[118:121], v[18:25], v[210:217], 0
	v_mfma_f32_16x16x128_f8f6f4 v[114:117], v[26:33], v[210:217], 0
	s_setprio 0
	s_setprio 1
	v_mfma_f32_16x16x128_f8f6f4 v[142:145], v[2:9], v[182:189], 0
	v_mfma_f32_16x16x128_f8f6f4 v[138:141], v[10:17], v[182:189], 0
	v_mfma_f32_16x16x128_f8f6f4 v[134:137], v[2:9], v[194:201], 0
	v_mfma_f32_16x16x128_f8f6f4 v[126:129], v[10:17], v[194:201], 0
	v_mfma_f32_16x16x128_f8f6f4 v[110:113], v[2:9], v[202:209], 0
	v_mfma_f32_16x16x128_f8f6f4 v[106:109], v[10:17], v[202:209], 0
	v_mfma_f32_16x16x128_f8f6f4 v[102:105], v[2:9], v[210:217], 0
	v_mfma_f32_16x16x128_f8f6f4 v[98:101], v[10:17], v[210:217], 0
	s_setprio 0
	s_barrier
	s_add_i32 s84, s76, s60
	v_lshl_add_u64 v[182:183], s[50:51], 0, v[166:167]
	s_mov_b32 m0, s84
	ds_read_b128 v[194:197], v192 offset:16384
	ds_read_b128 v[198:201], v192 offset:17408
	ds_read_b128 v[202:205], v192 offset:18432
	ds_read_b128 v[206:209], v192 offset:19456
	ds_read_b128 v[210:213], v192 offset:20480
	ds_read_b128 v[214:217], v192 offset:21504
	ds_read_b128 v[218:221], v192 offset:22528
	ds_read_b128 v[222:225], v192 offset:23552
	global_load_lds_dwordx4 v[182:183], off
	s_add_i32 m0, s84, 0x2000
	s_add_u32 s84, s50, 0x20000
	v_lshl_add_u64 v[184:185], s[50:51], 0, v[162:163]
	s_addc_u32 s85, s51, 0
	s_add_i32 s86, s77, s60
	global_load_lds_dwordx4 v[184:185], off
	v_lshl_add_u64 v[186:187], s[84:85], 0, v[166:167]
	s_mov_b32 m0, s86
	v_lshl_add_u64 v[188:189], s[52:53], 0, v[164:165]
	global_load_lds_dwordx4 v[186:187], off
	v_lshl_add_u64 v[186:187], s[84:85], 0, v[162:163]
	s_add_i32 m0, s86, 0x2000
	s_nop 0
	global_load_lds_dwordx4 v[186:187], off
	v_lshl_add_u64 v[186:187], s[52:53], 0, v[168:169]
	s_mov_b32 m0, s62
	s_nop 0
	global_load_lds_dwordx4 v[186:187], off
	s_mov_b32 m0, s63
	s_nop 0
	global_load_lds_dwordx4 v[188:189], off
	s_waitcnt vmcnt(8)
	s_waitcnt lgkmcnt(0)
	s_barrier
	s_setprio 1
	s_waitcnt lgkmcnt(0)
	v_mfma_f32_16x16x128_f8f6f4 v[94:97], v[18:25], v[194:201], 0
	v_mfma_f32_16x16x128_f8f6f4 v[90:93], v[26:33], v[194:201], 0
	v_mfma_f32_16x16x128_f8f6f4 v[86:89], v[18:25], v[202:209], 0
	v_mfma_f32_16x16x128_f8f6f4 v[82:85], v[26:33], v[202:209], 0
	v_mfma_f32_16x16x128_f8f6f4 v[66:69], v[18:25], v[210:217], 0
	v_mfma_f32_16x16x128_f8f6f4 v[58:61], v[26:33], v[210:217], 0
	v_mfma_f32_16x16x128_f8f6f4 v[54:57], v[18:25], v[218:225], 0
	v_mfma_f32_16x16x128_f8f6f4 v[50:53], v[26:33], v[218:225], 0
	s_setprio 0
	s_setprio 1
	v_mfma_f32_16x16x128_f8f6f4 v[78:81], v[2:9], v[194:201], 0
	v_mfma_f32_16x16x128_f8f6f4 v[74:77], v[10:17], v[194:201], 0
	v_mfma_f32_16x16x128_f8f6f4 v[70:73], v[2:9], v[202:209], 0
	v_mfma_f32_16x16x128_f8f6f4 v[62:65], v[10:17], v[202:209], 0
	v_mfma_f32_16x16x128_f8f6f4 v[46:49], v[2:9], v[210:217], 0
	v_mfma_f32_16x16x128_f8f6f4 v[42:45], v[10:17], v[210:217], 0
	v_mfma_f32_16x16x128_f8f6f4 v[38:41], v[2:9], v[218:225], 0
	v_mfma_f32_16x16x128_f8f6f4 v[34:37], v[10:17], v[218:225], 0
	s_setprio 0
	s_barrier
; #define PG8_STAGE(bufoff, gbase, voff) do { _Pragma("unroll") for (int _i = 0; _i < 2; ++_i) \
;         __builtin_amdgcn_global_load_lds((const unsigned*)((const char*)(gbase) + (voff)[_i]), (PG8_LAS unsigned*)(lds + (bufoff) + ldsw + _i * 8192), 16, 0, 0); } while (0)
; #define PG8_STAGE_A(bufoff, kbase, h, gv) do { if constexpr (GATHER) { PG8_STAGE(bufoff, kbase, (gv)[h]); } else { PG8_STAGE(bufoff, (kbase) + (h) * hstep, voffA); } } while (0)
; #define PG8_WAIT_V(n) asm volatile("s_waitcnt vmcnt(" #n ")" ::: "memory")
; #define PG8_WAIT_L(n) asm volatile("s_waitcnt lgkmcnt(" #n ")" ::: "memory")
; #define PG8_BAR __builtin_amdgcn_s_barrier()
; #define PG8_SCHED __builtin_amdgcn_sched_barrier(0)
; template <class Epi, class Sched, bool ALIGN_EPI = false, bool SP2 = false, bool FP8 = false, bool GATHER = false>
; __device__ __forceinline__ void gemm_phase(PG8_LAS unsigned char* lds, const Gemm g, const Sched& S, const Epi& E) {
;     ...
;         for (int t = 0; t < nt; t += 2) {
;     ...
;             PG8_LDB(B0, 1, 0); PG8_LDB(B1, 1, 1); PG8_SCHED; PG8_LDA(At, 1, 0); PG8_STAGE_A(PG8_SA(0, 1), a2, 1, gsel);
;             PG8_WAIT_V(8); PG8_WAIT_L(0); PG8_BAR; PG8_MMA(0, 0, At, B0); PG8_MMA(0, 1, At, B1); PG8_BAR; PG8_SCHED;
;             PG8_LDA(At, 1, 1); PG8_STAGE(PG8_SB(1, 0), b3, voffB); PG8_STAGE(PG8_SB(1, 1), b3 + hstep, voffB); PG8_STAGE_A(PG8_SA(1, 0), a3, 0, gsel);
;             PG8_WAIT_V(8); PG8_WAIT_L(0); PG8_BAR; PG8_MMA(1, 0, At, B0); PG8_MMA(1, 1, At, B1); PG8_BAR; PG8_SCHED;
	s_add_i32 s84, 0, 0x18000
	s_add_i32 s85, 0, 0x1c000
	v_add_u32_e32 v14, s84, v191
	v_add_u32_e32 v30, s85, v191
	ds_read_b128 v[2:5], v14
	ds_read_b128 v[6:9], v14 offset:1024
	ds_read_b128 v[10:13], v14 offset:2048
	ds_read_b128 v[14:17], v14 offset:3072
	ds_read_b128 v[18:21], v30
	ds_read_b128 v[22:25], v30 offset:1024
	ds_read_b128 v[26:29], v30 offset:2048
	ds_read_b128 v[30:33], v30 offset:3072
	s_add_u32 s52, s52, 0x20000
	s_addc_u32 s53, s53, 0
	s_mov_b32 m0, s65
	v_lshl_add_u64 v[226:227], s[52:53], 0, v[168:169]
	ds_read_b128 v[194:197], v192 offset:32768
	ds_read_b128 v[198:201], v192 offset:33792
	ds_read_b128 v[202:205], v192 offset:34816
	ds_read_b128 v[206:209], v192 offset:35840
	ds_read_b128 v[210:213], v192 offset:36864
	ds_read_b128 v[214:217], v192 offset:37888
	ds_read_b128 v[218:221], v192 offset:38912
	ds_read_b128 v[222:225], v192 offset:39936
	global_load_lds_dwordx4 v[226:227], off
	v_lshl_add_u64 v[226:227], s[52:53], 0, v[164:165]
	s_mov_b32 m0, s66
	s_nop 0
	global_load_lds_dwordx4 v[226:227], off
	s_waitcnt vmcnt(8)
	s_waitcnt lgkmcnt(0)
	s_barrier
	s_setprio 1
	s_waitcnt lgkmcnt(0)
	v_mfma_f32_16x16x128_f8f6f4 v[158:161], v[2:9], v[194:201], v[158:161]
	v_mfma_f32_16x16x128_f8f6f4 v[154:157], v[10:17], v[194:201], v[154:157]
	v_mfma_f32_16x16x128_f8f6f4 v[150:153], v[2:9], v[202:209], v[150:153]
	v_mfma_f32_16x16x128_f8f6f4 v[146:149], v[10:17], v[202:209], v[146:149]
	v_mfma_f32_16x16x128_f8f6f4 v[130:133], v[2:9], v[210:217], v[130:133]
	v_mfma_f32_16x16x128_f8f6f4 v[122:125], v[10:17], v[210:217], v[122:125]
	v_mfma_f32_16x16x128_f8f6f4 v[118:121], v[2:9], v[218:225], v[118:121]
	v_mfma_f32_16x16x128_f8f6f4 v[114:117], v[10:17], v[218:225], v[114:117]
	s_setprio 0
	s_setprio 1
	v_mfma_f32_16x16x128_f8f6f4 v[142:145], v[18:25], v[194:201], v[142:145]
	v_mfma_f32_16x16x128_f8f6f4 v[138:141], v[26:33], v[194:201], v[138:141]
	v_mfma_f32_16x16x128_f8f6f4 v[134:137], v[18:25], v[202:209], v[134:137]
	v_mfma_f32_16x16x128_f8f6f4 v[126:129], v[26:33], v[202:209], v[126:129]
	v_mfma_f32_16x16x128_f8f6f4 v[110:113], v[18:25], v[210:217], v[110:113]
	v_mfma_f32_16x16x128_f8f6f4 v[106:109], v[26:33], v[210:217], v[106:109]
	v_mfma_f32_16x16x128_f8f6f4 v[102:105], v[18:25], v[218:225], v[102:105]
	v_mfma_f32_16x16x128_f8f6f4 v[98:101], v[26:33], v[218:225], v[98:101]
	s_setprio 0
	s_barrier
	s_add_i32 s52, s84, s60
	v_lshl_add_u64 v[182:183], v[182:183], 0, s[18:19]
	s_mov_b32 m0, s52
	ds_read_b128 v[194:197], v192 offset:49152
	ds_read_b128 v[198:201], v192 offset:50176
	ds_read_b128 v[202:205], v192 offset:51200
	ds_read_b128 v[206:209], v192 offset:52224
	ds_read_b128 v[210:213], v192 offset:53248
	ds_read_b128 v[214:217], v192 offset:54272
	ds_read_b128 v[218:221], v192 offset:55296
	ds_read_b128 v[222:225], v192 offset:56320
	global_load_lds_dwordx4 v[182:183], off
	s_add_i32 m0, s52, 0x2000
	s_add_u32 s50, s50, 0x20080
	v_lshl_add_u64 v[182:183], v[184:185], 0, s[18:19]
	s_addc_u32 s51, s51, 0
	s_add_i32 s52, s85, s60
	global_load_lds_dwordx4 v[182:183], off
	v_lshl_add_u64 v[182:183], s[50:51], 0, v[166:167]
	s_mov_b32 m0, s52
	s_nop 0
	global_load_lds_dwordx4 v[182:183], off
	v_lshl_add_u64 v[182:183], s[50:51], 0, v[162:163]
	s_add_i32 m0, s52, 0x2000
	s_nop 0
	global_load_lds_dwordx4 v[182:183], off
	v_lshl_add_u64 v[182:183], v[186:187], 0, s[18:19]
	s_mov_b32 m0, s69
	s_nop 0
	global_load_lds_dwordx4 v[182:183], off
	v_lshl_add_u64 v[182:183], v[188:189], 0, s[18:19]
	s_mov_b32 m0, s70
	s_nop 0
	global_load_lds_dwordx4 v[182:183], off
	s_waitcnt vmcnt(8)
	s_waitcnt lgkmcnt(0)
	s_barrier
	s_setprio 1
	s_waitcnt lgkmcnt(0)
	v_mfma_f32_16x16x128_f8f6f4 v[94:97], v[2:9], v[194:201], v[94:97]
	v_mfma_f32_16x16x128_f8f6f4 v[90:93], v[10:17], v[194:201], v[90:93]
	v_mfma_f32_16x16x128_f8f6f4 v[86:89], v[2:9], v[202:209], v[86:89]
	v_mfma_f32_16x16x128_f8f6f4 v[82:85], v[10:17], v[202:209], v[82:85]
	v_mfma_f32_16x16x128_f8f6f4 v[66:69], v[2:9], v[210:217], v[66:69]
	v_mfma_f32_16x16x128_f8f6f4 v[58:61], v[10:17], v[210:217], v[58:61]
	v_mfma_f32_16x16x128_f8f6f4 v[54:57], v[2:9], v[218:225], v[54:57]
	v_mfma_f32_16x16x128_f8f6f4 v[50:53], v[10:17], v[218:225], v[50:53]
	s_setprio 0
	s_setprio 1
	v_mfma_f32_16x16x128_f8f6f4 v[78:81], v[18:25], v[194:201], v[78:81]
	v_mfma_f32_16x16x128_f8f6f4 v[74:77], v[26:33], v[194:201], v[74:77]
	v_mfma_f32_16x16x128_f8f6f4 v[70:73], v[18:25], v[202:209], v[70:73]
	v_mfma_f32_16x16x128_f8f6f4 v[62:65], v[26:33], v[202:209], v[62:65]
	v_mfma_f32_16x16x128_f8f6f4 v[46:49], v[18:25], v[210:217], v[46:49]
	v_mfma_f32_16x16x128_f8f6f4 v[42:45], v[26:33], v[210:217], v[42:45]
	v_mfma_f32_16x16x128_f8f6f4 v[38:41], v[18:25], v[218:225], v[38:41]
	v_mfma_f32_16x16x128_f8f6f4 v[34:37], v[26:33], v[218:225], v[34:37]
	s_setprio 0
	s_barrier
	s_add_i32 s83, s83, 2
	s_add_u32 s48, s48, 0x100
	s_addc_u32 s49, s49, 0
	s_add_u32 s47, s47, 0x100
	s_addc_u32 s82, s82, 0
	s_cmp_gt_u32 s83, 5
	s_cbranch_scc1 .LBB0_962
	s_branch .LBB0_954

; #define PG8_STAGE(bufoff, gbase, voff) do { _Pragma("unroll") for (int _i = 0; _i < 2; ++_i) \
;         __builtin_amdgcn_global_load_lds((const unsigned*)((const char*)(gbase) + (voff)[_i]), (PG8_LAS unsigned*)(lds + (bufoff) + ldsw + _i * 8192), 16, 0, 0); } while (0)
; #define PG8_STAGE_A(bufoff, kbase, h, gv) do { if constexpr (GATHER) { PG8_STAGE(bufoff, kbase, (gv)[h]); } else { PG8_STAGE(bufoff, (kbase) + (h) * hstep, voffA); } } while (0)
; #define PG8_WAIT_V(n) asm volatile("s_waitcnt vmcnt(" #n ")" ::: "memory")
; #define PG8_WAIT_L(n) asm volatile("s_waitcnt lgkmcnt(" #n ")" ::: "memory")
; #define PG8_BAR __builtin_amdgcn_s_barrier()
; #define PG8_SCHED __builtin_amdgcn_sched_barrier(0)
;     __device__ __forceinline__ int brow(const pg8::Unit& u) const { return (u.pn >> 8) * Nper + (u.pn & 255) * 256; }
; template <class Epi, class Sched, bool ALIGN_EPI = false, bool SP2 = false, bool FP8 = false, bool GATHER = false>
; __device__ __forceinline__ void gemm_phase(PG8_LAS unsigned char* lds, const Gemm g, const Sched& S, const Epi& E) {
;     ...
;         const bool has_next = S.next(ui + 1, nxt);
;         const char* nA = (has_next && !GATHER) ? (const char*)g.A + (size_t)nxt.pm * tstep : cA; const char* nB = has_next ? (const char*)g.Bt + (size_t)S.brow(nxt) * (size_t)K * 2 : cB;
; #pragma nounroll
;         for (int t = 0; t < nt; t += 2) {
;             const bool last = (t == nt - 2);
;             const char* a1 = cA + (size_t)(t + 1) * kstep;
;             const char* a2 = last ? nA : cA + (size_t)(t + 2) * kstep; const char* b2 = last ? nB : cB + (size_t)(t + 2) * kstep;
;     ...
;             PG8_LDB(B0, 0, 0); PG8_LDB(B1, 0, 1); PG8_SCHED; PG8_LDA(At, 0, 0); PG8_STAGE_A(PG8_SA(1, 1), a1, 1, gcur);
;             PG8_WAIT_V(8); PG8_WAIT_L(0); PG8_BAR; PG8_MMA(0, 0, At, B0); PG8_MMA(0, 1, At, B1); PG8_BAR; PG8_SCHED;
;             PG8_LDA(At, 0, 1); PG8_STAGE(PG8_SB(0, 0), b2, voffB); PG8_STAGE(PG8_SB(0, 1), b2 + hstep, voffB); PG8_STAGE_A(PG8_SA(0, 0), a2, 0, gsel);
;             PG8_WAIT_V(8); PG8_WAIT_L(0); PG8_BAR; PG8_MMA(1, 0, At, B0); PG8_MMA(1, 1, At, B1); PG8_BAR; PG8_SCHED;
.LBB0_1127:
	s_mov_b32 s46, s7
	s_ashr_i32 s47, s7, 31
	s_lshl_b64 s[12:13], s[46:47], 19
	s_add_u32 s50, s65, s12
	s_addc_u32 s51, s66, s13
	s_mov_b32 s95, s14
	s_and_b64 s[12:13], s[48:49], exec
	s_cselect_b32 s7, s51, s9
	s_cselect_b32 s14, s50, s8
	s_lshl_b32 s12, s95, 8
	s_ashr_i32 s13, s12, 31
	s_lshl_b64 s[12:13], s[12:13], 11
	s_add_u32 s52, s67, s12
	s_addc_u32 s53, s68, s13
	s_and_b64 s[12:13], s[48:49], exec
	s_cselect_b32 s15, s53, s11
	s_cselect_b32 s16, s52, s10
	s_add_u32 s8, s8, 0x40080
	s_addc_u32 s9, s9, 0
	s_add_u32 s17, s10, 0x100
	s_addc_u32 s18, s11, 0
	s_mov_b32 s47, -2
	ds_read_b128 v[74:77], v164
	ds_read_b128 v[78:81], v164 offset:1024
	ds_read_b128 v[152:155], v164 offset:2048
	ds_read_b128 v[156:159], v164 offset:3072
	ds_read_b128 v[170:173], v165
	ds_read_b128 v[174:177], v165 offset:1024
	ds_read_b128 v[178:181], v165 offset:2048
	ds_read_b128 v[182:185], v165 offset:3072
	s_add_u32 s10, s8, 0xfffc0080
	s_addc_u32 s11, s9, -1
	s_cmp_eq_u32 s47, 12
	s_cselect_b32 s13, s7, s11
	s_cselect_b32 s12, s14, s10
	s_cselect_b32 s11, s15, s18
	s_cselect_b32 s10, s16, s17
	v_lshl_add_u64 v[160:161], s[8:9], 0, v[146:147]
	s_add_i32 m0, s69, 0xc000
	ds_read_b128 v[186:189], v166
	ds_read_b128 v[190:193], v166 offset:1024
	ds_read_b128 v[194:197], v166 offset:2048
	ds_read_b128 v[198:201], v166 offset:3072
	ds_read_b128 v[202:205], v166 offset:4096
	ds_read_b128 v[206:209], v166 offset:5120
	ds_read_b128 v[210:213], v166 offset:6144
	ds_read_b128 v[214:217], v166 offset:7168
	global_load_lds_dwordx4 v[160:161], off
	v_lshl_add_u64 v[160:161], s[8:9], 0, v[148:149]
	s_add_i32 m0, s69, 0xe000
	s_nop 0
	global_load_lds_dwordx4 v[160:161], off
	s_waitcnt vmcnt(8)
	s_waitcnt lgkmcnt(0)
	s_barrier
	s_setprio 1
	s_waitcnt lgkmcnt(0)
	v_mfma_f32_16x16x32_bf16 v[134:137], v[74:77], v[186:189], 0
	v_mfma_f32_16x16x32_bf16 v[130:133], v[152:155], v[186:189], 0
	v_mfma_f32_16x16x32_bf16 v[126:129], v[74:77], v[194:197], 0
	v_mfma_f32_16x16x32_bf16 v[122:125], v[152:155], v[194:197], 0
	v_mfma_f32_16x16x32_bf16 v[118:121], v[74:77], v[202:205], 0
	v_mfma_f32_16x16x32_bf16 v[114:117], v[152:155], v[202:205], 0
	v_mfma_f32_16x16x32_bf16 v[110:113], v[74:77], v[210:213], 0
	v_mfma_f32_16x16x32_bf16 v[106:109], v[152:155], v[210:213], 0
	v_mfma_f32_16x16x32_bf16 v[134:137], v[78:81], v[190:193], v[134:137]
	v_mfma_f32_16x16x32_bf16 v[130:133], v[156:159], v[190:193], v[130:133]
	v_mfma_f32_16x16x32_bf16 v[126:129], v[78:81], v[198:201], v[126:129]
	v_mfma_f32_16x16x32_bf16 v[122:125], v[156:159], v[198:201], v[122:125]
	v_mfma_f32_16x16x32_bf16 v[118:121], v[78:81], v[206:209], v[118:121]
	v_mfma_f32_16x16x32_bf16 v[114:117], v[156:159], v[206:209], v[114:117]
	v_mfma_f32_16x16x32_bf16 v[110:113], v[78:81], v[214:217], v[110:113]
	v_mfma_f32_16x16x32_bf16 v[106:109], v[156:159], v[214:217], v[106:109]
	s_setprio 0
	s_setprio 1
	v_mfma_f32_16x16x32_bf16 v[62:65], v[170:173], v[186:189], 0
	v_mfma_f32_16x16x32_bf16 v[58:61], v[178:181], v[186:189], 0
	v_mfma_f32_16x16x32_bf16 v[54:57], v[170:173], v[194:197], 0
	v_mfma_f32_16x16x32_bf16 v[50:53], v[178:181], v[194:197], 0
	v_mfma_f32_16x16x32_bf16 v[46:49], v[170:173], v[202:205], 0
	v_mfma_f32_16x16x32_bf16 v[42:45], v[178:181], v[202:205], 0
	v_mfma_f32_16x16x32_bf16 v[38:41], v[170:173], v[210:213], 0
	v_mfma_f32_16x16x32_bf16 v[34:37], v[178:181], v[210:213], 0
	v_mfma_f32_16x16x32_bf16 v[62:65], v[174:177], v[190:193], v[62:65]
	v_mfma_f32_16x16x32_bf16 v[58:61], v[182:185], v[190:193], v[58:61]
	v_mfma_f32_16x16x32_bf16 v[54:57], v[174:177], v[198:201], v[54:57]
	v_mfma_f32_16x16x32_bf16 v[50:53], v[182:185], v[198:201], v[50:53]
	v_mfma_f32_16x16x32_bf16 v[46:49], v[174:177], v[206:209], v[46:49]
	v_mfma_f32_16x16x32_bf16 v[42:45], v[182:185], v[206:209], v[42:45]
	v_mfma_f32_16x16x32_bf16 v[38:41], v[174:177], v[214:217], v[38:41]
	v_mfma_f32_16x16x32_bf16 v[34:37], v[182:185], v[214:217], v[34:37]
	s_setprio 0
	s_barrier
	s_add_i32 s55, s87, s45
	v_lshl_add_u64 v[160:161], s[10:11], 0, v[140:141]
	s_mov_b32 m0, s55
	ds_read_b128 v[186:189], v166 offset:16384
	ds_read_b128 v[190:193], v166 offset:17408
	ds_read_b128 v[194:197], v166 offset:18432
	ds_read_b128 v[198:201], v166 offset:19456
	ds_read_b128 v[202:205], v166 offset:20480
	ds_read_b128 v[206:209], v166 offset:21504
	ds_read_b128 v[210:213], v166 offset:22528
	ds_read_b128 v[214:217], v166 offset:23552
	global_load_lds_dwordx4 v[160:161], off
	s_add_i32 m0, s55, 0x2000
	s_add_u32 s56, s10, 0x40000
	v_lshl_add_u64 v[218:219], s[10:11], 0, v[144:145]
	s_addc_u32 s57, s11, 0
	s_add_i32 s55, s88, s45
	global_load_lds_dwordx4 v[218:219], off
	v_lshl_add_u64 v[220:221], s[56:57], 0, v[140:141]
	s_mov_b32 m0, s55
	v_lshl_add_u64 v[222:223], s[12:13], 0, v[142:143]
	global_load_lds_dwordx4 v[220:221], off
	v_lshl_add_u64 v[220:221], s[56:57], 0, v[144:145]
	s_add_i32 m0, s55, 0x2000
	s_nop 0
	global_load_lds_dwordx4 v[220:221], off
	v_lshl_add_u64 v[220:221], s[12:13], 0, v[138:139]
	s_mov_b32 m0, s69
	s_nop 0
	global_load_lds_dwordx4 v[220:221], off
	s_mov_b32 m0, s70
	s_nop 0
	global_load_lds_dwordx4 v[222:223], off
	s_waitcnt vmcnt(8)
	s_waitcnt lgkmcnt(0)
	s_barrier
; #define PG8_STAGE_A(bufoff, kbase, h, gv) do { if constexpr (GATHER) { PG8_STAGE(bufoff, kbase, (gv)[h]); } else { PG8_STAGE(bufoff, (kbase) + (h) * hstep, voffA); } } while (0)
; #define PG8_WAIT_V(n) asm volatile("s_waitcnt vmcnt(" #n ")" ::: "memory")
; #define PG8_WAIT_L(n) asm volatile("s_waitcnt lgkmcnt(" #n ")" ::: "memory")
; #define PG8_BAR __builtin_amdgcn_s_barrier()
; #define PG8_SCHED __builtin_amdgcn_sched_barrier(0)
; template <class Epi, class Sched, bool ALIGN_EPI = false, bool SP2 = false, bool FP8 = false, bool GATHER = false>
; __device__ __forceinline__ void gemm_phase(PG8_LAS unsigned char* lds, const Gemm g, const Sched& S, const Epi& E) {
;     ...
;             PG8_WAIT_V(8); PG8_WAIT_L(0); PG8_BAR; PG8_MMA(1, 0, At, B0); PG8_MMA(1, 1, At, B1); PG8_BAR; PG8_SCHED;
;             PG8_LDB(B0, 1, 0); PG8_LDB(B1, 1, 1); PG8_SCHED; PG8_LDA(At, 1, 0); PG8_STAGE_A(PG8_SA(0, 1), a2, 1, gsel);
;             PG8_WAIT_V(8); PG8_WAIT_L(0); PG8_BAR; PG8_MMA(0, 0, At, B0); PG8_MMA(0, 1, At, B1); PG8_BAR; PG8_SCHED;
	s_setprio 1
	s_waitcnt lgkmcnt(0)
	v_mfma_f32_16x16x32_bf16 v[102:105], v[74:77], v[186:189], 0
	v_mfma_f32_16x16x32_bf16 v[98:101], v[152:155], v[186:189], 0
	v_mfma_f32_16x16x32_bf16 v[94:97], v[74:77], v[194:197], 0
	v_mfma_f32_16x16x32_bf16 v[90:93], v[152:155], v[194:197], 0
	v_mfma_f32_16x16x32_bf16 v[86:89], v[74:77], v[202:205], 0
	v_mfma_f32_16x16x32_bf16 v[82:85], v[152:155], v[202:205], 0
	v_mfma_f32_16x16x32_bf16 v[70:73], v[74:77], v[210:213], 0
	v_mfma_f32_16x16x32_bf16 v[66:69], v[152:155], v[210:213], 0
	v_mfma_f32_16x16x32_bf16 v[102:105], v[78:81], v[190:193], v[102:105]
	v_mfma_f32_16x16x32_bf16 v[98:101], v[156:159], v[190:193], v[98:101]
	v_mfma_f32_16x16x32_bf16 v[94:97], v[78:81], v[198:201], v[94:97]
	v_mfma_f32_16x16x32_bf16 v[90:93], v[156:159], v[198:201], v[90:93]
	v_mfma_f32_16x16x32_bf16 v[86:89], v[78:81], v[206:209], v[86:89]
	v_mfma_f32_16x16x32_bf16 v[82:85], v[156:159], v[206:209], v[82:85]
	v_mfma_f32_16x16x32_bf16 v[70:73], v[78:81], v[214:217], v[70:73]
	v_mfma_f32_16x16x32_bf16 v[66:69], v[156:159], v[214:217], v[66:69]
	s_setprio 0
	s_setprio 1
	v_mfma_f32_16x16x32_bf16 v[30:33], v[170:173], v[186:189], 0
	v_mfma_f32_16x16x32_bf16 v[26:29], v[178:181], v[186:189], 0
	v_mfma_f32_16x16x32_bf16 v[22:25], v[170:173], v[194:197], 0
	v_mfma_f32_16x16x32_bf16 v[18:21], v[178:181], v[194:197], 0
	v_mfma_f32_16x16x32_bf16 v[14:17], v[170:173], v[202:205], 0
	v_mfma_f32_16x16x32_bf16 v[10:13], v[178:181], v[202:205], 0
	v_mfma_f32_16x16x32_bf16 v[6:9], v[170:173], v[210:213], 0
	v_mfma_f32_16x16x32_bf16 v[2:5], v[178:181], v[210:213], 0
	v_mfma_f32_16x16x32_bf16 v[30:33], v[174:177], v[190:193], v[30:33]
	v_mfma_f32_16x16x32_bf16 v[26:29], v[182:185], v[190:193], v[26:29]
	v_mfma_f32_16x16x32_bf16 v[22:25], v[174:177], v[198:201], v[22:25]
	v_mfma_f32_16x16x32_bf16 v[18:21], v[182:185], v[198:201], v[18:21]
	v_mfma_f32_16x16x32_bf16 v[14:17], v[174:177], v[206:209], v[14:17]
	v_mfma_f32_16x16x32_bf16 v[10:13], v[182:185], v[206:209], v[10:13]
	v_mfma_f32_16x16x32_bf16 v[6:9], v[174:177], v[214:217], v[6:9]
	v_mfma_f32_16x16x32_bf16 v[2:5], v[182:185], v[214:217], v[2:5]
	s_setprio 0
	s_barrier
	s_add_i32 s55, 0, 0x18000
	s_add_i32 s56, 0, 0x1c000
	v_add_u32_e32 v156, s55, v163
	v_add_u32_e32 v182, s56, v163
	ds_read_b128 v[74:77], v156
	ds_read_b128 v[78:81], v156 offset:1024
	ds_read_b128 v[152:155], v156 offset:2048
	ds_read_b128 v[156:159], v156 offset:3072
	ds_read_b128 v[170:173], v182
	ds_read_b128 v[174:177], v182 offset:1024
	ds_read_b128 v[178:181], v182 offset:2048
	ds_read_b128 v[182:185], v182 offset:3072
	s_add_u32 s12, s12, 0x40000
	s_addc_u32 s13, s13, 0
	s_mov_b32 m0, s71
	v_lshl_add_u64 v[224:225], s[12:13], 0, v[138:139]
	ds_read_b128 v[186:189], v166 offset:32768
	ds_read_b128 v[190:193], v166 offset:33792
	ds_read_b128 v[194:197], v166 offset:34816
	ds_read_b128 v[198:201], v166 offset:35840
	ds_read_b128 v[202:205], v166 offset:36864
	ds_read_b128 v[206:209], v166 offset:37888
	ds_read_b128 v[210:213], v166 offset:38912
	ds_read_b128 v[214:217], v166 offset:39936
	global_load_lds_dwordx4 v[224:225], off
	v_lshl_add_u64 v[224:225], s[12:13], 0, v[142:143]
	s_mov_b32 m0, s72
	s_nop 0
	global_load_lds_dwordx4 v[224:225], off
	s_waitcnt vmcnt(8)
	s_waitcnt lgkmcnt(0)
	s_barrier
	s_setprio 1
	s_waitcnt lgkmcnt(0)
	v_mfma_f32_16x16x32_bf16 v[134:137], v[74:77], v[186:189], v[134:137]
	v_mfma_f32_16x16x32_bf16 v[130:133], v[152:155], v[186:189], v[130:133]
	v_mfma_f32_16x16x32_bf16 v[126:129], v[74:77], v[194:197], v[126:129]
	v_mfma_f32_16x16x32_bf16 v[122:125], v[152:155], v[194:197], v[122:125]
	v_mfma_f32_16x16x32_bf16 v[118:121], v[74:77], v[202:205], v[118:121]
	v_mfma_f32_16x16x32_bf16 v[114:117], v[152:155], v[202:205], v[114:117]
	v_mfma_f32_16x16x32_bf16 v[110:113], v[74:77], v[210:213], v[110:113]
	v_mfma_f32_16x16x32_bf16 v[106:109], v[152:155], v[210:213], v[106:109]
	v_mfma_f32_16x16x32_bf16 v[134:137], v[78:81], v[190:193], v[134:137]
	v_mfma_f32_16x16x32_bf16 v[130:133], v[156:159], v[190:193], v[130:133]
	v_mfma_f32_16x16x32_bf16 v[126:129], v[78:81], v[198:201], v[126:129]
	v_mfma_f32_16x16x32_bf16 v[122:125], v[156:159], v[198:201], v[122:125]
	v_mfma_f32_16x16x32_bf16 v[118:121], v[78:81], v[206:209], v[118:121]
	v_mfma_f32_16x16x32_bf16 v[114:117], v[156:159], v[206:209], v[114:117]
	v_mfma_f32_16x16x32_bf16 v[110:113], v[78:81], v[214:217], v[110:113]
	v_mfma_f32_16x16x32_bf16 v[106:109], v[156:159], v[214:217], v[106:109]
	s_setprio 0
	s_setprio 1
	v_mfma_f32_16x16x32_bf16 v[62:65], v[170:173], v[186:189], v[62:65]
	v_mfma_f32_16x16x32_bf16 v[58:61], v[178:181], v[186:189], v[58:61]
	v_mfma_f32_16x16x32_bf16 v[54:57], v[170:173], v[194:197], v[54:57]
	v_mfma_f32_16x16x32_bf16 v[50:53], v[178:181], v[194:197], v[50:53]
	v_mfma_f32_16x16x32_bf16 v[46:49], v[170:173], v[202:205], v[46:49]
	v_mfma_f32_16x16x32_bf16 v[42:45], v[178:181], v[202:205], v[42:45]
	v_mfma_f32_16x16x32_bf16 v[38:41], v[170:173], v[210:213], v[38:41]
	v_mfma_f32_16x16x32_bf16 v[34:37], v[178:181], v[210:213], v[34:37]
	v_mfma_f32_16x16x32_bf16 v[62:65], v[174:177], v[190:193], v[62:65]
	v_mfma_f32_16x16x32_bf16 v[58:61], v[182:185], v[190:193], v[58:61]
	v_mfma_f32_16x16x32_bf16 v[54:57], v[174:177], v[198:201], v[54:57]
	v_mfma_f32_16x16x32_bf16 v[50:53], v[182:185], v[198:201], v[50:53]
	v_mfma_f32_16x16x32_bf16 v[46:49], v[174:177], v[206:209], v[46:49]
	v_mfma_f32_16x16x32_bf16 v[42:45], v[182:185], v[206:209], v[42:45]
	v_mfma_f32_16x16x32_bf16 v[38:41], v[174:177], v[214:217], v[38:41]
	v_mfma_f32_16x16x32_bf16 v[34:37], v[182:185], v[214:217], v[34:37]
	s_setprio 0
	s_barrier
; #define PG8_STAGE(bufoff, gbase, voff) do { _Pragma("unroll") for (int _i = 0; _i < 2; ++_i) \
;         __builtin_amdgcn_global_load_lds((const unsigned*)((const char*)(gbase) + (voff)[_i]), (PG8_LAS unsigned*)(lds + (bufoff) + ldsw + _i * 8192), 16, 0, 0); } while (0)
; #define PG8_STAGE_A(bufoff, kbase, h, gv) do { if constexpr (GATHER) { PG8_STAGE(bufoff, kbase, (gv)[h]); } else { PG8_STAGE(bufoff, (kbase) + (h) * hstep, voffA); } } while (0)
; #define PG8_WAIT_V(n) asm volatile("s_waitcnt vmcnt(" #n ")" ::: "memory")
; #define PG8_WAIT_L(n) asm volatile("s_waitcnt lgkmcnt(" #n ")" ::: "memory")
; #define PG8_BAR __builtin_amdgcn_s_barrier()
; #define PG8_SCHED __builtin_amdgcn_sched_barrier(0)
; template <class Epi, class Sched, bool ALIGN_EPI = false, bool SP2 = false, bool FP8 = false, bool GATHER = false>
; __device__ __forceinline__ void gemm_phase(PG8_LAS unsigned char* lds, const Gemm g, const Sched& S, const Epi& E) {
;     ...
;         for (int t = 0; t < nt; t += 2) {
;     ...
;             PG8_LDA(At, 1, 1); PG8_STAGE(PG8_SB(1, 0), b3, voffB); PG8_STAGE(PG8_SB(1, 1), b3 + hstep, voffB); PG8_STAGE_A(PG8_SA(1, 0), a3, 0, gsel);
;             PG8_WAIT_V(8); PG8_WAIT_L(0); PG8_BAR; PG8_MMA(1, 0, At, B0); PG8_MMA(1, 1, At, B1); PG8_BAR; PG8_SCHED;
	s_add_i32 s12, s55, s45
	v_lshl_add_u64 v[160:161], v[160:161], 0, s[28:29]
	s_mov_b32 m0, s12
	ds_read_b128 v[186:189], v166 offset:49152
	ds_read_b128 v[190:193], v166 offset:50176
	ds_read_b128 v[194:197], v166 offset:51200
	ds_read_b128 v[198:201], v166 offset:52224
	ds_read_b128 v[202:205], v166 offset:53248
	ds_read_b128 v[206:209], v166 offset:54272
	ds_read_b128 v[210:213], v166 offset:55296
	ds_read_b128 v[214:217], v166 offset:56320
	global_load_lds_dwordx4 v[160:161], off
	s_add_i32 m0, s12, 0x2000
	s_add_u32 s10, s10, 0x40080
	v_lshl_add_u64 v[160:161], v[218:219], 0, s[28:29]
	s_addc_u32 s11, s11, 0
	s_add_i32 s12, s56, s45
	global_load_lds_dwordx4 v[160:161], off
	v_lshl_add_u64 v[160:161], s[10:11], 0, v[140:141]
	s_mov_b32 m0, s12
	s_nop 0
	global_load_lds_dwordx4 v[160:161], off
	v_lshl_add_u64 v[160:161], s[10:11], 0, v[144:145]
	s_add_i32 m0, s12, 0x2000
	s_nop 0
	global_load_lds_dwordx4 v[160:161], off
	v_lshl_add_u64 v[160:161], v[220:221], 0, s[28:29]
	s_mov_b32 m0, s79
	s_nop 0
	global_load_lds_dwordx4 v[160:161], off
	v_lshl_add_u64 v[160:161], v[222:223], 0, s[28:29]
	s_mov_b32 m0, s80
	s_nop 0
	global_load_lds_dwordx4 v[160:161], off
	s_waitcnt vmcnt(8)
	s_waitcnt lgkmcnt(0)
	s_barrier
	s_setprio 1
	s_waitcnt lgkmcnt(0)
	v_mfma_f32_16x16x32_bf16 v[102:105], v[74:77], v[186:189], v[102:105]
	v_mfma_f32_16x16x32_bf16 v[98:101], v[152:155], v[186:189], v[98:101]
	v_mfma_f32_16x16x32_bf16 v[94:97], v[74:77], v[194:197], v[94:97]
	v_mfma_f32_16x16x32_bf16 v[90:93], v[152:155], v[194:197], v[90:93]
	v_mfma_f32_16x16x32_bf16 v[86:89], v[74:77], v[202:205], v[86:89]
	v_mfma_f32_16x16x32_bf16 v[82:85], v[152:155], v[202:205], v[82:85]
	v_mfma_f32_16x16x32_bf16 v[70:73], v[74:77], v[210:213], v[70:73]
	v_mfma_f32_16x16x32_bf16 v[66:69], v[152:155], v[210:213], v[66:69]
	v_mfma_f32_16x16x32_bf16 v[102:105], v[78:81], v[190:193], v[102:105]
	v_mfma_f32_16x16x32_bf16 v[98:101], v[156:159], v[190:193], v[98:101]
	v_mfma_f32_16x16x32_bf16 v[94:97], v[78:81], v[198:201], v[94:97]
	v_mfma_f32_16x16x32_bf16 v[90:93], v[156:159], v[198:201], v[90:93]
	v_mfma_f32_16x16x32_bf16 v[86:89], v[78:81], v[206:209], v[86:89]
	v_mfma_f32_16x16x32_bf16 v[82:85], v[156:159], v[206:209], v[82:85]
	v_mfma_f32_16x16x32_bf16 v[70:73], v[78:81], v[214:217], v[70:73]
	v_mfma_f32_16x16x32_bf16 v[66:69], v[156:159], v[214:217], v[66:69]
	s_setprio 0
	s_setprio 1
	v_mfma_f32_16x16x32_bf16 v[30:33], v[170:173], v[186:189], v[30:33]
	v_mfma_f32_16x16x32_bf16 v[26:29], v[178:181], v[186:189], v[26:29]
	v_mfma_f32_16x16x32_bf16 v[22:25], v[170:173], v[194:197], v[22:25]
	v_mfma_f32_16x16x32_bf16 v[18:21], v[178:181], v[194:197], v[18:21]
	v_mfma_f32_16x16x32_bf16 v[14:17], v[170:173], v[202:205], v[14:17]
	v_mfma_f32_16x16x32_bf16 v[10:13], v[178:181], v[202:205], v[10:13]
	v_mfma_f32_16x16x32_bf16 v[6:9], v[170:173], v[210:213], v[6:9]
	v_mfma_f32_16x16x32_bf16 v[2:5], v[178:181], v[210:213], v[2:5]
	v_mfma_f32_16x16x32_bf16 v[30:33], v[174:177], v[190:193], v[30:33]
	v_mfma_f32_16x16x32_bf16 v[26:29], v[182:185], v[190:193], v[26:29]
	v_mfma_f32_16x16x32_bf16 v[22:25], v[174:177], v[198:201], v[22:25]
	v_mfma_f32_16x16x32_bf16 v[18:21], v[182:185], v[198:201], v[18:21]
	v_mfma_f32_16x16x32_bf16 v[14:17], v[174:177], v[206:209], v[14:17]
	v_mfma_f32_16x16x32_bf16 v[10:13], v[182:185], v[206:209], v[10:13]
	v_mfma_f32_16x16x32_bf16 v[6:9], v[174:177], v[214:217], v[6:9]
	v_mfma_f32_16x16x32_bf16 v[2:5], v[182:185], v[214:217], v[2:5]
	s_setprio 0
	s_barrier
	s_add_i32 s47, s47, 2
	s_add_u32 s8, s8, 0x100
	s_addc_u32 s9, s9, 0
	s_add_u32 s17, s17, 0x100
	s_addc_u32 s18, s18, 0
	s_cmp_gt_u32 s47, 13

;     __device__ __forceinline__ int brow(const pg8::Unit& u) const { return (u.pn >> 8) * Nper + (u.pn & 255) * 256; }
; template <class Epi, class Sched, bool ALIGN_EPI = false, bool SP2 = false, bool FP8 = false, bool GATHER = false>
; __device__ __forceinline__ void gemm_phase(PG8_LAS unsigned char* lds, const Gemm g, const Sched& S, const Epi& E) {
;     ...
;         const bool has_next = S.next(ui + 1, nxt);
;         const char* nA = (has_next && !GATHER) ? (const char*)g.A + (size_t)nxt.pm * tstep : cA; const char* nB = has_next ? (const char*)g.Bt + (size_t)S.brow(nxt) * (size_t)K * 2 : cB;
; #pragma nounroll
;         for (int t = 0; t < nt; t += 2) {
;             const bool last = (t == nt - 2);
;             const char* a1 = cA + (size_t)(t + 1) * kstep;
;             const char* a2 = last ? nA : cA + (size_t)(t + 2) * kstep; const char* b2 = last ? nB : cB + (size_t)(t + 2) * kstep;
;             const char* a3 = a2 + kstep; const char* b3 = b2 + kstep;
;             if (last && has_next) S.a_ready(nxt);
;             if (last) E.pre(cur, wid, lane);
;             if constexpr (GATHER) { if (t == nt - 4 && has_next) { _Pragma("unroll") for (int h_ = 0; h_ < 2; ++h_) _Pragma("unroll") for (int i_ = 0; i_ < 2; ++i_)
;                 asm volatile("global_load_dword %0, %1, off" : "+v"(graw[h_][i_]) : "v"(S.rowtok + (nxt.pm * BM + h_ * HALF + gR[i_])) : "memory"); } }
;             unsigned gsel[2][2];
;             if constexpr (GATHER) { _Pragma("unroll") for (int h_ = 0; h_ < 2; ++h_) _Pragma("unroll") for (int i_ = 0; i_ < 2; ++i_) { if (last && has_next) gnxt[h_][i_] = graw[h_][i_] * (unsigned)(K * 2) + gC[i_]; gsel[h_][i_] = (last && has_next) ? gnxt[h_][i_] : gcur[h_][i_]; } }
.LBB0_1780:
	s_ashr_i32 s50, s48, 8
	s_ashr_i32 s51, s50, 31
	s_lshl_b32 s20, s48, 7
	s_lshl_b64 s[50:51], s[50:51], 13
	s_and_b32 s81, s20, 0x7f80
	s_lshl_b32 s48, s78, 8
	v_lshl_add_u64 v[6:7], v[172:173], 0, s[50:51]
	s_lshl_b32 s20, s81, 2
	v_lshl_add_u64 v[6:7], v[6:7], 0, s[20:21]
	s_ashr_i32 s49, s48, 31
	v_lshl_add_u64 v[182:183], v[6:7], 0, v[174:175]
	v_lshl_add_u64 v[6:7], s[48:49], 0, v[164:165]
	v_lshl_add_u64 v[6:7], v[6:7], 2, s[10:11]
	v_add_u32_e32 v2, s48, v162
	v_add_u32_e32 v4, s48, v164
	v_lshl_add_u64 v[184:185], v[6:7], 0, s[26:27]
	v_lshl_add_u64 v[6:7], s[48:49], 0, v[162:163]
	v_ashrrev_i32_e32 v3, 31, v2
	v_ashrrev_i32_e32 v5, 31, v4
	v_mov_b32_e32 v179, v171
	v_mov_b32_e32 v177, v171
	v_lshl_add_u64 v[6:7], v[6:7], 2, s[10:11]
	s_add_u32 s20, s46, 0x100
	v_lshl_add_u64 v[186:187], v[6:7], 0, s[26:27]
	v_lshl_add_u64 v[188:189], v[4:5], 2, s[10:11]
	v_lshl_add_u64 v[190:191], v[2:3], 2, s[10:11]
	v_lshl_add_u64 v[192:193], s[18:19], 0, v[176:177]
	v_lshl_add_u64 v[194:195], s[18:19], 0, v[178:179]
	s_addc_u32 s82, s47, 0
	s_mov_b32 s83, -2
	s_mov_b64 s[46:47], 0
	s_xor_b64 s[48:49], s[44:45], -1

; #define PG8_STAGE(bufoff, gbase, voff) do { _Pragma("unroll") for (int _i = 0; _i < 2; ++_i) \
;         __builtin_amdgcn_global_load_lds((const unsigned*)((const char*)(gbase) + (voff)[_i]), (PG8_LAS unsigned*)(lds + (bufoff) + ldsw + _i * 8192), 16, 0, 0); } while (0)
; #define PG8_STAGE_A(bufoff, kbase, h, gv) do { if constexpr (GATHER) { PG8_STAGE(bufoff, kbase, (gv)[h]); } else { PG8_STAGE(bufoff, (kbase) + (h) * hstep, voffA); } } while (0)
; #define PG8_WAIT_V(n) asm volatile("s_waitcnt vmcnt(" #n ")" ::: "memory")
; #define PG8_WAIT_L(n) asm volatile("s_waitcnt lgkmcnt(" #n ")" ::: "memory")
; #define PG8_BAR __builtin_amdgcn_s_barrier()
; #define PG8_SCHED __builtin_amdgcn_sched_barrier(0)
; template <class Epi, class Sched, bool ALIGN_EPI = false, bool SP2 = false, bool FP8 = false, bool GATHER = false>
; __device__ __forceinline__ void gemm_phase(PG8_LAS unsigned char* lds, const Gemm g, const Sched& S, const Epi& E) {
;     ...
;             if constexpr (GATHER) { _Pragma("unroll") for (int h_ = 0; h_ < 2; ++h_) _Pragma("unroll") for (int i_ = 0; i_ < 2; ++i_) { if (last && has_next) gnxt[h_][i_] = graw[h_][i_] * (unsigned)(K * 2) + gC[i_]; gsel[h_][i_] = (last && has_next) ? gnxt[h_][i_] : gcur[h_][i_]; } }
;             if constexpr (SP2) {
;             PG8_LDB(B0, 0, 0); PG8_LDB(B1, 0, 1); PG8_SCHED; PG8_LDA(At, 0, 0); PG8_STAGE_A(PG8_SA(1, 1), a1, 1, gcur);
;             PG8_WAIT_V(8); PG8_WAIT_L(0); PG8_BAR; PG8_MMA(0, 0, At, B0); PG8_MMA(0, 1, At, B1); PG8_BAR; PG8_SCHED;
;             PG8_LDA(At, 0, 1); PG8_STAGE(PG8_SB(0, 0), b2, voffB); PG8_STAGE(PG8_SB(0, 1), b2 + hstep, voffB); PG8_STAGE_A(PG8_SA(0, 0), a2, 0, gsel);
;             PG8_WAIT_V(8); PG8_WAIT_L(0); PG8_BAR; PG8_MMA(1, 0, At, B0); PG8_MMA(1, 1, At, B1); PG8_BAR; PG8_SCHED;
.Lpeel1781_body:
	s_add_u32 s50, s6, s46
	s_addc_u32 s51, s7, s47
	s_add_u32 s52, s50, 0x19200100
	s_addc_u32 s53, s51, 0
	s_and_b64 s[50:51], s[54:55], exec
	s_cselect_b32 s53, s9, s53
	s_cselect_b32 s52, s8, s52
	s_add_u32 s84, s20, s46
	s_addc_u32 s85, s82, s47
	s_and_b64 s[50:51], s[54:55], exec
	s_cselect_b32 s51, s35, s85
	s_cselect_b32 s50, s34, s84
	v_lshl_add_u32 v2, v213, 10, v1
	s_and_b64 vcc, s[44:45], s[54:55]
	v_cndmask_b32_e32 v209, v209, v2, vcc
	v_cndmask_b32_e32 v170, v217, v2, vcc
	v_lshl_add_u32 v2, v214, 10, v204
	v_cndmask_b32_e32 v210, v210, v2, vcc
	v_cndmask_b32_e32 v200, v180, v2, vcc
	v_add_u32_e32 v2, s74, v206
	v_add_u32_e32 v14, s75, v206
	ds_read_b128 v[18:21], v2
	ds_read_b128 v[22:25], v2 offset:1024
	ds_read_b128 v[26:29], v2 offset:2048
	ds_read_b128 v[30:33], v2 offset:3072
	ds_read_b128 v[2:5], v14
	ds_read_b128 v[6:9], v14 offset:1024
	ds_read_b128 v[10:13], v14 offset:2048
	ds_read_b128 v[14:17], v14 offset:3072
	v_lshl_add_u32 v177, v215, 10, v1
	v_lshl_add_u32 v179, v216, 10, v204
	v_cndmask_b32_e32 v211, v211, v177, vcc
	v_cndmask_b32_e32 v212, v212, v179, vcc
	v_cndmask_b32_e32 v177, v178, v177, vcc
	v_cndmask_b32_e32 v179, v176, v179, vcc
	v_lshl_add_u64 v[196:197], v[194:195], 0, s[46:47]
	s_add_i32 m0, s61, 0xc000
	ds_read_b128 v[218:221], v207
	ds_read_b128 v[222:225], v207 offset:1024
	ds_read_b128 v[226:229], v207 offset:2048
	ds_read_b128 v[230:233], v207 offset:3072
	ds_read_b128 v[234:237], v207 offset:4096
	ds_read_b128 v[238:241], v207 offset:5120
	ds_read_b128 v[242:245], v207 offset:6144
	ds_read_b128 v[246:249], v207 offset:7168
	global_load_lds_dwordx4 v[196:197], off
	v_lshl_add_u64 v[196:197], v[192:193], 0, s[46:47]
	s_add_i32 m0, s61, 0xe000
	s_nop 0
	global_load_lds_dwordx4 v[196:197], off
	s_waitcnt vmcnt(8)
	s_waitcnt lgkmcnt(0)
	s_barrier
	s_setprio 1
	s_waitcnt lgkmcnt(0)
	v_mfma_f32_16x16x128_f8f6f4 v[158:161], v[18:25], v[218:225], 0
	v_mfma_f32_16x16x128_f8f6f4 v[150:153], v[26:33], v[218:225], 0
	v_mfma_f32_16x16x128_f8f6f4 v[142:145], v[18:25], v[226:233], 0
	v_mfma_f32_16x16x128_f8f6f4 v[134:137], v[26:33], v[226:233], 0
	v_mfma_f32_16x16x128_f8f6f4 v[126:129], v[18:25], v[234:241], 0
	v_mfma_f32_16x16x128_f8f6f4 v[118:121], v[26:33], v[234:241], 0
	v_mfma_f32_16x16x128_f8f6f4 v[110:113], v[18:25], v[242:249], 0
	v_mfma_f32_16x16x128_f8f6f4 v[102:105], v[26:33], v[242:249], 0
	s_setprio 0
	s_setprio 1
	v_mfma_f32_16x16x128_f8f6f4 v[154:157], v[2:9], v[218:225], 0
	v_mfma_f32_16x16x128_f8f6f4 v[146:149], v[10:17], v[218:225], 0
	v_mfma_f32_16x16x128_f8f6f4 v[138:141], v[2:9], v[226:233], 0
	v_mfma_f32_16x16x128_f8f6f4 v[130:133], v[10:17], v[226:233], 0
	v_mfma_f32_16x16x128_f8f6f4 v[122:125], v[2:9], v[234:241], 0
	v_mfma_f32_16x16x128_f8f6f4 v[114:117], v[10:17], v[234:241], 0
	v_mfma_f32_16x16x128_f8f6f4 v[106:109], v[2:9], v[242:249], 0
	v_mfma_f32_16x16x128_f8f6f4 v[98:101], v[10:17], v[242:249], 0
	s_setprio 0
	s_barrier
	s_add_i32 s54, s74, s58
	v_lshl_add_u64 v[196:197], s[50:51], 0, v[168:169]
	s_mov_b32 m0, s54
	ds_read_b128 v[218:221], v207 offset:16384
	ds_read_b128 v[222:225], v207 offset:17408
	ds_read_b128 v[226:229], v207 offset:18432
	ds_read_b128 v[230:233], v207 offset:19456
	ds_read_b128 v[234:237], v207 offset:20480
	ds_read_b128 v[238:241], v207 offset:21504
	ds_read_b128 v[242:245], v207 offset:22528
	ds_read_b128 v[246:249], v207 offset:23552
	global_load_lds_dwordx4 v[196:197], off
	s_add_i32 m0, s54, 0x2000
	s_add_u32 s54, s50, 0x20000
	v_lshl_add_u64 v[198:199], s[50:51], 0, v[166:167]
	s_addc_u32 s55, s51, 0
	s_add_i32 s84, s75, s58
	global_load_lds_dwordx4 v[198:199], off
	v_lshl_add_u64 v[202:203], s[54:55], 0, v[168:169]
	s_mov_b32 m0, s84
	v_mov_b32_e32 v201, v171
	global_load_lds_dwordx4 v[202:203], off
	v_lshl_add_u64 v[202:203], s[54:55], 0, v[166:167]
	s_add_i32 m0, s84, 0x2000
	s_nop 0
	global_load_lds_dwordx4 v[202:203], off
	s_mov_b32 m0, s61
	v_lshl_add_u64 v[202:203], s[52:53], 0, v[170:171]
	global_load_lds_dwordx4 v170, s[52:53]
	s_mov_b32 m0, s62
	s_nop 0
	global_load_lds_dwordx4 v200, s[52:53]
	s_waitcnt vmcnt(8)
	s_waitcnt lgkmcnt(0)
	v_lshl_add_u64 v[200:201], s[52:53], 0, v[200:201]
	s_barrier
	s_setprio 1
	s_waitcnt lgkmcnt(0)
	v_mfma_f32_16x16x128_f8f6f4 v[94:97], v[18:25], v[218:225], 0
	v_mfma_f32_16x16x128_f8f6f4 v[86:89], v[26:33], v[218:225], 0
	v_mfma_f32_16x16x128_f8f6f4 v[78:81], v[18:25], v[226:233], 0
	v_mfma_f32_16x16x128_f8f6f4 v[70:73], v[26:33], v[226:233], 0
	v_mfma_f32_16x16x128_f8f6f4 v[62:65], v[18:25], v[234:241], 0
	v_mfma_f32_16x16x128_f8f6f4 v[54:57], v[26:33], v[234:241], 0
	v_mfma_f32_16x16x128_f8f6f4 v[46:49], v[18:25], v[242:249], 0
	v_mfma_f32_16x16x128_f8f6f4 v[38:41], v[26:33], v[242:249], 0
	s_setprio 0
	s_setprio 1
	v_mfma_f32_16x16x128_f8f6f4 v[90:93], v[2:9], v[218:225], 0
	v_mfma_f32_16x16x128_f8f6f4 v[82:85], v[10:17], v[218:225], 0
	v_mfma_f32_16x16x128_f8f6f4 v[74:77], v[2:9], v[226:233], 0
	v_mfma_f32_16x16x128_f8f6f4 v[66:69], v[10:17], v[226:233], 0
	v_mfma_f32_16x16x128_f8f6f4 v[58:61], v[2:9], v[234:241], 0
	v_mfma_f32_16x16x128_f8f6f4 v[50:53], v[10:17], v[234:241], 0
	v_mfma_f32_16x16x128_f8f6f4 v[42:45], v[2:9], v[242:249], 0
	v_mfma_f32_16x16x128_f8f6f4 v[34:37], v[10:17], v[242:249], 0
	s_setprio 0
	s_barrier
; #define PG8_STAGE(bufoff, gbase, voff) do { _Pragma("unroll") for (int _i = 0; _i < 2; ++_i) \
;         __builtin_amdgcn_global_load_lds((const unsigned*)((const char*)(gbase) + (voff)[_i]), (PG8_LAS unsigned*)(lds + (bufoff) + ldsw + _i * 8192), 16, 0, 0); } while (0)
; #define PG8_STAGE_A(bufoff, kbase, h, gv) do { if constexpr (GATHER) { PG8_STAGE(bufoff, kbase, (gv)[h]); } else { PG8_STAGE(bufoff, (kbase) + (h) * hstep, voffA); } } while (0)
; #define PG8_WAIT_V(n) asm volatile("s_waitcnt vmcnt(" #n ")" ::: "memory")
; #define PG8_WAIT_L(n) asm volatile("s_waitcnt lgkmcnt(" #n ")" ::: "memory")
; #define PG8_BAR __builtin_amdgcn_s_barrier()
; #define PG8_SCHED __builtin_amdgcn_sched_barrier(0)
; template <class Epi, class Sched, bool ALIGN_EPI = false, bool SP2 = false, bool FP8 = false, bool GATHER = false>
; __device__ __forceinline__ void gemm_phase(PG8_LAS unsigned char* lds, const Gemm g, const Sched& S, const Epi& E) {
;     ...
;         for (int t = 0; t < nt; t += 2) {
;     ...
;             PG8_LDB(B0, 1, 0); PG8_LDB(B1, 1, 1); PG8_SCHED; PG8_LDA(At, 1, 0); PG8_STAGE_A(PG8_SA(0, 1), a2, 1, gsel);
;             PG8_WAIT_V(8); PG8_WAIT_L(0); PG8_BAR; PG8_MMA(0, 0, At, B0); PG8_MMA(0, 1, At, B1); PG8_BAR; PG8_SCHED;
;             PG8_LDA(At, 1, 1); PG8_STAGE(PG8_SB(1, 0), b3, voffB); PG8_STAGE(PG8_SB(1, 1), b3 + hstep, voffB); PG8_STAGE_A(PG8_SA(1, 0), a3, 0, gsel);
;             PG8_WAIT_V(8); PG8_WAIT_L(0); PG8_BAR; PG8_MMA(1, 0, At, B0); PG8_MMA(1, 1, At, B1); PG8_BAR; PG8_SCHED;
	s_add_i32 s54, 0, 0x18000
	s_add_i32 s55, 0, 0x1c000
	v_add_u32_e32 v14, s54, v206
	v_add_u32_e32 v30, s55, v206
	ds_read_b128 v[2:5], v14
	ds_read_b128 v[6:9], v14 offset:1024
	ds_read_b128 v[10:13], v14 offset:2048
	ds_read_b128 v[14:17], v14 offset:3072
	ds_read_b128 v[18:21], v30
	ds_read_b128 v[22:25], v30 offset:1024
	ds_read_b128 v[26:29], v30 offset:2048
	ds_read_b128 v[30:33], v30 offset:3072
	s_mov_b32 m0, s63
	ds_read_b128 v[218:221], v207 offset:32768
	ds_read_b128 v[222:225], v207 offset:33792
	ds_read_b128 v[226:229], v207 offset:34816
	ds_read_b128 v[230:233], v207 offset:35840
	ds_read_b128 v[234:237], v207 offset:36864
	ds_read_b128 v[238:241], v207 offset:37888
	ds_read_b128 v[242:245], v207 offset:38912
	ds_read_b128 v[246:249], v207 offset:39936
	global_load_lds_dwordx4 v177, s[52:53]
	s_mov_b32 m0, s65
	s_nop 0
	global_load_lds_dwordx4 v179, s[52:53]
	s_waitcnt vmcnt(8)
	s_waitcnt lgkmcnt(0)
	s_barrier
	s_setprio 1
	s_waitcnt lgkmcnt(0)
	v_mfma_f32_16x16x128_f8f6f4 v[158:161], v[2:9], v[218:225], v[158:161]
	v_mfma_f32_16x16x128_f8f6f4 v[150:153], v[10:17], v[218:225], v[150:153]
	v_mfma_f32_16x16x128_f8f6f4 v[142:145], v[2:9], v[226:233], v[142:145]
	v_mfma_f32_16x16x128_f8f6f4 v[134:137], v[10:17], v[226:233], v[134:137]
	v_mfma_f32_16x16x128_f8f6f4 v[126:129], v[2:9], v[234:241], v[126:129]
	v_mfma_f32_16x16x128_f8f6f4 v[118:121], v[10:17], v[234:241], v[118:121]
	v_mfma_f32_16x16x128_f8f6f4 v[110:113], v[2:9], v[242:249], v[110:113]
	v_mfma_f32_16x16x128_f8f6f4 v[102:105], v[10:17], v[242:249], v[102:105]
	s_setprio 0
	s_setprio 1
	v_mfma_f32_16x16x128_f8f6f4 v[154:157], v[18:25], v[218:225], v[154:157]
	v_mfma_f32_16x16x128_f8f6f4 v[146:149], v[26:33], v[218:225], v[146:149]
	v_mfma_f32_16x16x128_f8f6f4 v[138:141], v[18:25], v[226:233], v[138:141]
	v_mfma_f32_16x16x128_f8f6f4 v[130:133], v[26:33], v[226:233], v[130:133]
	v_mfma_f32_16x16x128_f8f6f4 v[122:125], v[18:25], v[234:241], v[122:125]
	v_mfma_f32_16x16x128_f8f6f4 v[114:117], v[26:33], v[234:241], v[114:117]
	v_mfma_f32_16x16x128_f8f6f4 v[106:109], v[18:25], v[242:249], v[106:109]
	v_mfma_f32_16x16x128_f8f6f4 v[98:101], v[26:33], v[242:249], v[98:101]
	s_setprio 0
	s_barrier
	s_add_i32 s52, s54, s58
	v_lshl_add_u64 v[196:197], v[196:197], 0, s[16:17]
	s_mov_b32 m0, s52
	ds_read_b128 v[218:221], v207 offset:49152
	ds_read_b128 v[222:225], v207 offset:50176
	ds_read_b128 v[226:229], v207 offset:51200
	ds_read_b128 v[230:233], v207 offset:52224
	ds_read_b128 v[234:237], v207 offset:53248
	ds_read_b128 v[238:241], v207 offset:54272
	ds_read_b128 v[242:245], v207 offset:55296
	ds_read_b128 v[246:249], v207 offset:56320
	global_load_lds_dwordx4 v[196:197], off
	s_add_i32 m0, s52, 0x2000
	s_add_u32 s50, s50, 0x20080
	v_lshl_add_u64 v[196:197], v[198:199], 0, s[16:17]
	s_addc_u32 s51, s51, 0
	s_add_i32 s52, s55, s58
	global_load_lds_dwordx4 v[196:197], off
	v_lshl_add_u64 v[196:197], s[50:51], 0, v[168:169]
	s_mov_b32 m0, s52
	s_nop 0
	global_load_lds_dwordx4 v[196:197], off
	v_lshl_add_u64 v[196:197], s[50:51], 0, v[166:167]
	s_add_i32 m0, s52, 0x2000
	s_nop 0
	global_load_lds_dwordx4 v[196:197], off
	v_lshl_add_u64 v[196:197], v[202:203], 0, s[16:17]
	s_mov_b32 m0, s68
	s_nop 0
	global_load_lds_dwordx4 v[196:197], off
	v_lshl_add_u64 v[196:197], v[200:201], 0, s[16:17]
	s_mov_b32 m0, s69
	s_nop 0
	global_load_lds_dwordx4 v[196:197], off
	s_waitcnt vmcnt(8)
	s_waitcnt lgkmcnt(0)
	s_barrier
	s_setprio 1
	s_waitcnt lgkmcnt(0)
	v_mfma_f32_16x16x128_f8f6f4 v[94:97], v[2:9], v[218:225], v[94:97]
	v_mfma_f32_16x16x128_f8f6f4 v[86:89], v[10:17], v[218:225], v[86:89]
	v_mfma_f32_16x16x128_f8f6f4 v[78:81], v[2:9], v[226:233], v[78:81]
	v_mfma_f32_16x16x128_f8f6f4 v[70:73], v[10:17], v[226:233], v[70:73]
	v_mfma_f32_16x16x128_f8f6f4 v[62:65], v[2:9], v[234:241], v[62:65]
	v_mfma_f32_16x16x128_f8f6f4 v[54:57], v[10:17], v[234:241], v[54:57]
	v_mfma_f32_16x16x128_f8f6f4 v[46:49], v[2:9], v[242:249], v[46:49]
	v_mfma_f32_16x16x128_f8f6f4 v[38:41], v[10:17], v[242:249], v[38:41]
	s_setprio 0
	s_setprio 1
	v_mfma_f32_16x16x128_f8f6f4 v[90:93], v[18:25], v[218:225], v[90:93]
	v_mfma_f32_16x16x128_f8f6f4 v[82:85], v[26:33], v[218:225], v[82:85]
	v_mfma_f32_16x16x128_f8f6f4 v[74:77], v[18:25], v[226:233], v[74:77]
	v_mfma_f32_16x16x128_f8f6f4 v[66:69], v[26:33], v[226:233], v[66:69]
	v_mfma_f32_16x16x128_f8f6f4 v[58:61], v[18:25], v[234:241], v[58:61]
	v_mfma_f32_16x16x128_f8f6f4 v[50:53], v[26:33], v[234:241], v[50:53]
	v_mfma_f32_16x16x128_f8f6f4 v[42:45], v[18:25], v[242:249], v[42:45]
	v_mfma_f32_16x16x128_f8f6f4 v[34:37], v[26:33], v[242:249], v[34:37]
	s_setprio 0
	s_barrier
	s_add_i32 s83, s83, 2
	s_add_u32 s46, s46, 0x100
	s_addc_u32 s47, s47, 0
	s_cmp_gt_u32 s83, 5
	s_cbranch_scc1 .LBB0_1786
	s_branch .LBB0_1782

;     __device__ __forceinline__ int brow(const pg8::Unit& u) const { return (u.pn >> 8) * Nper + (u.pn & 255) * 256; }
; template <class Epi, class Sched, bool ALIGN_EPI = false, bool SP2 = false, bool FP8 = false, bool GATHER = false>
; __device__ __forceinline__ void gemm_phase(PG8_LAS unsigned char* lds, const Gemm g, const Sched& S, const Epi& E) {
;     ...
;         const bool has_next = S.next(ui + 1, nxt);
;         const char* nA = (has_next && !GATHER) ? (const char*)g.A + (size_t)nxt.pm * tstep : cA; const char* nB = has_next ? (const char*)g.Bt + (size_t)S.brow(nxt) * (size_t)K * 2 : cB;
; #pragma nounroll
;         for (int t = 0; t < nt; t += 2) {
;             const bool last = (t == nt - 2);
;             const char* a1 = cA + (size_t)(t + 1) * kstep;
;             const char* a2 = last ? nA : cA + (size_t)(t + 2) * kstep; const char* b2 = last ? nB : cB + (size_t)(t + 2) * kstep;
;     ...
;         for (int a = 0; a < 2; ++a)
; #pragma unroll
;             for (int b = 0; b < 2; ++b)
; #pragma unroll
;                 for (int m = 0; m < 4; ++m)
; #pragma unroll
;                     for (int n = 0; n < 2; ++n) acc[a][b][m][n] = (f32x4){0.f, 0.f, 0.f, 0.f};
;         cur = nxt; cA = nA; cB = nB; ++ui;
.LBB0_1855:
	s_ashr_i32 s27, s26, 31
	s_lshl_b64 s[28:29], s[26:27], 18
	s_add_u32 s28, s51, s28
	s_addc_u32 s29, s52, s29
	s_and_b64 s[78:79], s[30:31], exec
	s_cselect_b32 s78, s29, s45
	s_cselect_b32 s79, s28, s44
	s_ashr_i32 s82, s48, 8
	s_ashr_i32 s35, s34, 31
	s_ashr_i32 s83, s82, 31
	s_lshl_b32 s27, s48, 8
	s_lshl_b64 s[80:81], s[34:35], 10
	s_lshl_b64 s[82:83], s[82:83], 12
	s_and_b32 s27, s27, 0xff00
	s_add_u32 s35, s62, s82
	s_addc_u32 s49, s63, s83
	s_lshl_b32 s48, s27, 2
	s_add_u32 s48, s35, s48
	s_addc_u32 s49, s49, 0
	s_add_u32 s44, s44, 0x20080
	s_addc_u32 s45, s45, 0
	s_add_u32 s35, s46, 0x100
	v_lshl_add_u64 v[178:179], v[170:171], 0, s[80:81]
	v_lshl_add_u64 v[180:181], s[48:49], 0, v[176:177]
	s_addc_u32 s80, s47, 0
	s_mov_b32 s81, -2

; #define PG8_STAGE(bufoff, gbase, voff) do { _Pragma("unroll") for (int _i = 0; _i < 2; ++_i) \
;         __builtin_amdgcn_global_load_lds((const unsigned*)((const char*)(gbase) + (voff)[_i]), (PG8_LAS unsigned*)(lds + (bufoff) + ldsw + _i * 8192), 16, 0, 0); } while (0)
; #define PG8_STAGE_A(bufoff, kbase, h, gv) do { if constexpr (GATHER) { PG8_STAGE(bufoff, kbase, (gv)[h]); } else { PG8_STAGE(bufoff, (kbase) + (h) * hstep, voffA); } } while (0)
; #define PG8_WAIT_V(n) asm volatile("s_waitcnt vmcnt(" #n ")" ::: "memory")
; #define PG8_WAIT_L(n) asm volatile("s_waitcnt lgkmcnt(" #n ")" ::: "memory")
; #define PG8_BAR __builtin_amdgcn_s_barrier()
; #define PG8_SCHED __builtin_amdgcn_sched_barrier(0)
; template <class Epi, class Sched, bool ALIGN_EPI = false, bool SP2 = false, bool FP8 = false, bool GATHER = false>
; __device__ __forceinline__ void gemm_phase(PG8_LAS unsigned char* lds, const Gemm g, const Sched& S, const Epi& E) {
;     ...
;             PG8_LDB(B0, 0, 0); PG8_LDB(B1, 0, 1); PG8_SCHED; PG8_LDA(At, 0, 0); PG8_STAGE_A(PG8_SA(1, 1), a1, 1, gcur);
;             PG8_WAIT_V(8); PG8_WAIT_L(0); PG8_BAR; PG8_MMA(0, 0, At, B0); PG8_MMA(0, 1, At, B1); PG8_BAR; PG8_SCHED;
;             PG8_LDA(At, 0, 1); PG8_STAGE(PG8_SB(0, 0), b2, voffB); PG8_STAGE(PG8_SB(0, 1), b2 + hstep, voffB); PG8_STAGE_A(PG8_SA(0, 0), a2, 0, gsel);
;             PG8_WAIT_V(8); PG8_WAIT_L(0); PG8_BAR; PG8_MMA(1, 0, At, B0); PG8_MMA(1, 1, At, B1); PG8_BAR; PG8_SCHED;
.Lpeel1856_body:
	v_add_u32_e32 v2, s74, v191
	v_add_u32_e32 v14, s75, v191
	ds_read_b128 v[18:21], v2
	ds_read_b128 v[22:25], v2 offset:1024
	ds_read_b128 v[26:29], v2 offset:2048
	ds_read_b128 v[30:33], v2 offset:3072
	ds_read_b128 v[2:5], v14
	ds_read_b128 v[6:9], v14 offset:1024
	ds_read_b128 v[10:13], v14 offset:2048
	ds_read_b128 v[14:17], v14 offset:3072
	s_add_u32 s48, s44, 0xfffe0080
	s_addc_u32 s49, s45, -1
	s_and_b64 s[46:47], s[46:47], exec
	s_cselect_b32 s49, s78, s49
	s_cselect_b32 s48, s79, s48
	s_cselect_b32 s47, s25, s80
	s_cselect_b32 s46, s24, s35
	v_lshl_add_u64 v[218:219], s[44:45], 0, v[172:173]
	s_add_i32 m0, s58, 0xc000
	ds_read_b128 v[182:185], v192
	ds_read_b128 v[186:189], v192 offset:1024
	ds_read_b128 v[194:197], v192 offset:2048
	ds_read_b128 v[198:201], v192 offset:3072
	ds_read_b128 v[202:205], v192 offset:4096
	ds_read_b128 v[206:209], v192 offset:5120
	ds_read_b128 v[210:213], v192 offset:6144
	ds_read_b128 v[214:217], v192 offset:7168
	global_load_lds_dwordx4 v[218:219], off
	v_lshl_add_u64 v[218:219], s[44:45], 0, v[174:175]
	s_add_i32 m0, s58, 0xe000
	s_nop 0
	global_load_lds_dwordx4 v[218:219], off
	s_waitcnt vmcnt(8)
	s_waitcnt lgkmcnt(0)
	s_barrier
	s_setprio 1
	s_waitcnt lgkmcnt(0)
	v_mfma_f32_16x16x128_f8f6f4 v[158:161], v[18:25], v[182:189], 0
	v_mfma_f32_16x16x128_f8f6f4 v[154:157], v[26:33], v[182:189], 0
	v_mfma_f32_16x16x128_f8f6f4 v[150:153], v[18:25], v[194:201], 0
	v_mfma_f32_16x16x128_f8f6f4 v[146:149], v[26:33], v[194:201], 0
	v_mfma_f32_16x16x128_f8f6f4 v[130:133], v[18:25], v[202:209], 0
	v_mfma_f32_16x16x128_f8f6f4 v[122:125], v[26:33], v[202:209], 0
	v_mfma_f32_16x16x128_f8f6f4 v[118:121], v[18:25], v[210:217], 0
	v_mfma_f32_16x16x128_f8f6f4 v[114:117], v[26:33], v[210:217], 0
	s_setprio 0
	s_setprio 1
	v_mfma_f32_16x16x128_f8f6f4 v[142:145], v[2:9], v[182:189], 0
	v_mfma_f32_16x16x128_f8f6f4 v[138:141], v[10:17], v[182:189], 0
	v_mfma_f32_16x16x128_f8f6f4 v[134:137], v[2:9], v[194:201], 0
	v_mfma_f32_16x16x128_f8f6f4 v[126:129], v[10:17], v[194:201], 0
	v_mfma_f32_16x16x128_f8f6f4 v[110:113], v[2:9], v[202:209], 0
	v_mfma_f32_16x16x128_f8f6f4 v[106:109], v[10:17], v[202:209], 0
	v_mfma_f32_16x16x128_f8f6f4 v[102:105], v[2:9], v[210:217], 0
	v_mfma_f32_16x16x128_f8f6f4 v[98:101], v[10:17], v[210:217], 0
	s_setprio 0
	s_barrier
	s_add_i32 s82, s74, s56
	v_lshl_add_u64 v[182:183], s[46:47], 0, v[166:167]
	s_mov_b32 m0, s82
	ds_read_b128 v[194:197], v192 offset:16384
	ds_read_b128 v[198:201], v192 offset:17408
	ds_read_b128 v[202:205], v192 offset:18432
	ds_read_b128 v[206:209], v192 offset:19456
	ds_read_b128 v[210:213], v192 offset:20480
	ds_read_b128 v[214:217], v192 offset:21504
	ds_read_b128 v[218:221], v192 offset:22528
	ds_read_b128 v[222:225], v192 offset:23552
	global_load_lds_dwordx4 v[182:183], off
	s_add_i32 m0, s82, 0x2000
	s_add_u32 s82, s46, 0x20000
	v_lshl_add_u64 v[184:185], s[46:47], 0, v[162:163]
	s_addc_u32 s83, s47, 0
	s_add_i32 s84, s75, s56
	global_load_lds_dwordx4 v[184:185], off
	v_lshl_add_u64 v[186:187], s[82:83], 0, v[166:167]
	s_mov_b32 m0, s84
	v_lshl_add_u64 v[188:189], s[48:49], 0, v[164:165]
	global_load_lds_dwordx4 v[186:187], off
	v_lshl_add_u64 v[186:187], s[82:83], 0, v[162:163]
	s_add_i32 m0, s84, 0x2000
	s_nop 0
	global_load_lds_dwordx4 v[186:187], off
	v_lshl_add_u64 v[186:187], s[48:49], 0, v[168:169]
	s_mov_b32 m0, s58
	s_nop 0
	global_load_lds_dwordx4 v[186:187], off
	s_mov_b32 m0, s59
	s_nop 0
	global_load_lds_dwordx4 v[188:189], off
	s_waitcnt vmcnt(8)
	s_waitcnt lgkmcnt(0)
	s_barrier
	s_setprio 1
	s_waitcnt lgkmcnt(0)
	v_mfma_f32_16x16x128_f8f6f4 v[94:97], v[18:25], v[194:201], 0
	v_mfma_f32_16x16x128_f8f6f4 v[90:93], v[26:33], v[194:201], 0
	v_mfma_f32_16x16x128_f8f6f4 v[86:89], v[18:25], v[202:209], 0
	v_mfma_f32_16x16x128_f8f6f4 v[82:85], v[26:33], v[202:209], 0
	v_mfma_f32_16x16x128_f8f6f4 v[66:69], v[18:25], v[210:217], 0
	v_mfma_f32_16x16x128_f8f6f4 v[58:61], v[26:33], v[210:217], 0
	v_mfma_f32_16x16x128_f8f6f4 v[54:57], v[18:25], v[218:225], 0
	v_mfma_f32_16x16x128_f8f6f4 v[50:53], v[26:33], v[218:225], 0
	s_setprio 0
	s_setprio 1
	v_mfma_f32_16x16x128_f8f6f4 v[78:81], v[2:9], v[194:201], 0
	v_mfma_f32_16x16x128_f8f6f4 v[74:77], v[10:17], v[194:201], 0
	v_mfma_f32_16x16x128_f8f6f4 v[70:73], v[2:9], v[202:209], 0
	v_mfma_f32_16x16x128_f8f6f4 v[62:65], v[10:17], v[202:209], 0
	v_mfma_f32_16x16x128_f8f6f4 v[46:49], v[2:9], v[210:217], 0
	v_mfma_f32_16x16x128_f8f6f4 v[42:45], v[10:17], v[210:217], 0
	v_mfma_f32_16x16x128_f8f6f4 v[38:41], v[2:9], v[218:225], 0
	v_mfma_f32_16x16x128_f8f6f4 v[34:37], v[10:17], v[218:225], 0
	s_setprio 0
	s_barrier
; #define PG8_STAGE(bufoff, gbase, voff) do { _Pragma("unroll") for (int _i = 0; _i < 2; ++_i) \
;         __builtin_amdgcn_global_load_lds((const unsigned*)((const char*)(gbase) + (voff)[_i]), (PG8_LAS unsigned*)(lds + (bufoff) + ldsw + _i * 8192), 16, 0, 0); } while (0)
; #define PG8_STAGE_A(bufoff, kbase, h, gv) do { if constexpr (GATHER) { PG8_STAGE(bufoff, kbase, (gv)[h]); } else { PG8_STAGE(bufoff, (kbase) + (h) * hstep, voffA); } } while (0)
; #define PG8_WAIT_V(n) asm volatile("s_waitcnt vmcnt(" #n ")" ::: "memory")
; #define PG8_WAIT_L(n) asm volatile("s_waitcnt lgkmcnt(" #n ")" ::: "memory")
; #define PG8_BAR __builtin_amdgcn_s_barrier()
; #define PG8_SCHED __builtin_amdgcn_sched_barrier(0)
; template <class Epi, class Sched, bool ALIGN_EPI = false, bool SP2 = false, bool FP8 = false, bool GATHER = false>
; __device__ __forceinline__ void gemm_phase(PG8_LAS unsigned char* lds, const Gemm g, const Sched& S, const Epi& E) {
;     ...
;         for (int t = 0; t < nt; t += 2) {
;     ...
;             PG8_LDB(B0, 1, 0); PG8_LDB(B1, 1, 1); PG8_SCHED; PG8_LDA(At, 1, 0); PG8_STAGE_A(PG8_SA(0, 1), a2, 1, gsel);
;             PG8_WAIT_V(8); PG8_WAIT_L(0); PG8_BAR; PG8_MMA(0, 0, At, B0); PG8_MMA(0, 1, At, B1); PG8_BAR; PG8_SCHED;
;             PG8_LDA(At, 1, 1); PG8_STAGE(PG8_SB(1, 0), b3, voffB); PG8_STAGE(PG8_SB(1, 1), b3 + hstep, voffB); PG8_STAGE_A(PG8_SA(1, 0), a3, 0, gsel);
;             PG8_WAIT_V(8); PG8_WAIT_L(0); PG8_BAR; PG8_MMA(1, 0, At, B0); PG8_MMA(1, 1, At, B1); PG8_BAR; PG8_SCHED;
	s_add_i32 s82, 0, 0x18000
	s_add_i32 s83, 0, 0x1c000
	v_add_u32_e32 v14, s82, v191
	v_add_u32_e32 v30, s83, v191
	ds_read_b128 v[2:5], v14
	ds_read_b128 v[6:9], v14 offset:1024
	ds_read_b128 v[10:13], v14 offset:2048
	ds_read_b128 v[14:17], v14 offset:3072
	ds_read_b128 v[18:21], v30
	ds_read_b128 v[22:25], v30 offset:1024
	ds_read_b128 v[26:29], v30 offset:2048
	ds_read_b128 v[30:33], v30 offset:3072
	s_add_u32 s48, s48, 0x20000
	s_addc_u32 s49, s49, 0
	s_mov_b32 m0, s60
	v_lshl_add_u64 v[226:227], s[48:49], 0, v[168:169]
	ds_read_b128 v[194:197], v192 offset:32768
	ds_read_b128 v[198:201], v192 offset:33792
	ds_read_b128 v[202:205], v192 offset:34816
	ds_read_b128 v[206:209], v192 offset:35840
	ds_read_b128 v[210:213], v192 offset:36864
	ds_read_b128 v[214:217], v192 offset:37888
	ds_read_b128 v[218:221], v192 offset:38912
	ds_read_b128 v[222:225], v192 offset:39936
	global_load_lds_dwordx4 v[226:227], off
	v_lshl_add_u64 v[226:227], s[48:49], 0, v[164:165]
	s_mov_b32 m0, s61
	s_nop 0
	global_load_lds_dwordx4 v[226:227], off
	s_waitcnt vmcnt(8)
	s_waitcnt lgkmcnt(0)
	s_barrier
	s_setprio 1
	s_waitcnt lgkmcnt(0)
	v_mfma_f32_16x16x128_f8f6f4 v[158:161], v[2:9], v[194:201], v[158:161]
	v_mfma_f32_16x16x128_f8f6f4 v[154:157], v[10:17], v[194:201], v[154:157]
	v_mfma_f32_16x16x128_f8f6f4 v[150:153], v[2:9], v[202:209], v[150:153]
	v_mfma_f32_16x16x128_f8f6f4 v[146:149], v[10:17], v[202:209], v[146:149]
	v_mfma_f32_16x16x128_f8f6f4 v[130:133], v[2:9], v[210:217], v[130:133]
	v_mfma_f32_16x16x128_f8f6f4 v[122:125], v[10:17], v[210:217], v[122:125]
	v_mfma_f32_16x16x128_f8f6f4 v[118:121], v[2:9], v[218:225], v[118:121]
	v_mfma_f32_16x16x128_f8f6f4 v[114:117], v[10:17], v[218:225], v[114:117]
	s_setprio 0
	s_setprio 1
	v_mfma_f32_16x16x128_f8f6f4 v[142:145], v[18:25], v[194:201], v[142:145]
	v_mfma_f32_16x16x128_f8f6f4 v[138:141], v[26:33], v[194:201], v[138:141]
	v_mfma_f32_16x16x128_f8f6f4 v[134:137], v[18:25], v[202:209], v[134:137]
	v_mfma_f32_16x16x128_f8f6f4 v[126:129], v[26:33], v[202:209], v[126:129]
	v_mfma_f32_16x16x128_f8f6f4 v[110:113], v[18:25], v[210:217], v[110:113]
	v_mfma_f32_16x16x128_f8f6f4 v[106:109], v[26:33], v[210:217], v[106:109]
	v_mfma_f32_16x16x128_f8f6f4 v[102:105], v[18:25], v[218:225], v[102:105]
	v_mfma_f32_16x16x128_f8f6f4 v[98:101], v[26:33], v[218:225], v[98:101]
	s_setprio 0
	s_barrier
	s_add_i32 s48, s82, s56
	v_lshl_add_u64 v[182:183], v[182:183], 0, s[14:15]
	s_mov_b32 m0, s48
	ds_read_b128 v[194:197], v192 offset:49152
	ds_read_b128 v[198:201], v192 offset:50176
	ds_read_b128 v[202:205], v192 offset:51200
	ds_read_b128 v[206:209], v192 offset:52224
	ds_read_b128 v[210:213], v192 offset:53248
	ds_read_b128 v[214:217], v192 offset:54272
	ds_read_b128 v[218:221], v192 offset:55296
	ds_read_b128 v[222:225], v192 offset:56320
	global_load_lds_dwordx4 v[182:183], off
	s_add_i32 m0, s48, 0x2000
	s_add_u32 s46, s46, 0x20080
	v_lshl_add_u64 v[182:183], v[184:185], 0, s[14:15]
	s_addc_u32 s47, s47, 0
	s_add_i32 s48, s83, s56
	global_load_lds_dwordx4 v[182:183], off
	v_lshl_add_u64 v[182:183], s[46:47], 0, v[166:167]
	s_mov_b32 m0, s48
	s_nop 0
	global_load_lds_dwordx4 v[182:183], off
	v_lshl_add_u64 v[182:183], s[46:47], 0, v[162:163]
	s_add_i32 m0, s48, 0x2000
	s_nop 0
	global_load_lds_dwordx4 v[182:183], off
	v_lshl_add_u64 v[182:183], v[186:187], 0, s[14:15]
	s_mov_b32 m0, s67
	s_nop 0
	global_load_lds_dwordx4 v[182:183], off
	v_lshl_add_u64 v[182:183], v[188:189], 0, s[14:15]
	s_mov_b32 m0, s68
	s_nop 0
	global_load_lds_dwordx4 v[182:183], off
	s_waitcnt vmcnt(8)
	s_waitcnt lgkmcnt(0)
	s_barrier
	s_setprio 1
	s_waitcnt lgkmcnt(0)
	v_mfma_f32_16x16x128_f8f6f4 v[94:97], v[2:9], v[194:201], v[94:97]
	v_mfma_f32_16x16x128_f8f6f4 v[90:93], v[10:17], v[194:201], v[90:93]
	v_mfma_f32_16x16x128_f8f6f4 v[86:89], v[2:9], v[202:209], v[86:89]
	v_mfma_f32_16x16x128_f8f6f4 v[82:85], v[10:17], v[202:209], v[82:85]
	v_mfma_f32_16x16x128_f8f6f4 v[66:69], v[2:9], v[210:217], v[66:69]
	v_mfma_f32_16x16x128_f8f6f4 v[58:61], v[10:17], v[210:217], v[58:61]
	v_mfma_f32_16x16x128_f8f6f4 v[54:57], v[2:9], v[218:225], v[54:57]
	v_mfma_f32_16x16x128_f8f6f4 v[50:53], v[10:17], v[218:225], v[50:53]
	s_setprio 0
	s_setprio 1
	v_mfma_f32_16x16x128_f8f6f4 v[78:81], v[18:25], v[194:201], v[78:81]
	v_mfma_f32_16x16x128_f8f6f4 v[74:77], v[26:33], v[194:201], v[74:77]
	v_mfma_f32_16x16x128_f8f6f4 v[70:73], v[18:25], v[202:209], v[70:73]
	v_mfma_f32_16x16x128_f8f6f4 v[62:65], v[26:33], v[202:209], v[62:65]
	v_mfma_f32_16x16x128_f8f6f4 v[46:49], v[18:25], v[210:217], v[46:49]
	v_mfma_f32_16x16x128_f8f6f4 v[42:45], v[26:33], v[210:217], v[42:45]
	v_mfma_f32_16x16x128_f8f6f4 v[38:41], v[18:25], v[218:225], v[38:41]
	v_mfma_f32_16x16x128_f8f6f4 v[34:37], v[26:33], v[218:225], v[34:37]
	s_setprio 0
	s_barrier
	s_add_i32 s81, s81, 2
	s_add_u32 s44, s44, 0x100
	s_addc_u32 s45, s45, 0
	s_add_u32 s35, s35, 0x100
	s_addc_u32 s80, s80, 0
	s_cmp_gt_u32 s81, 5
	s_cbranch_scc1 .LBB0_1865
	s_branch .LBB0_1857
